# speedup vs baseline: 1.0984x; 1.0021x over previous
.LBB1_55:
	s_or_b64 exec, exec, s[2:3]
	v_and_b32_e32 v119, 63, v175
	v_lshlrev_b32_e32 v50, 2, v119
	v_add_u32_e32 v51, 0xffffff40, v50
	v_cmp_gt_u32_e32 vcc, 48, v119
	v_or_b32_e32 v111, 0x80, v119
	v_mul_lo_u16_e32 v111, 0xab, v111
	v_cndmask_b32_e32 v54, v51, v50, vcc
	v_or_b32_e32 v50, 64, v119
	v_mul_lo_u16_e32 v50, 43, v50
	v_lshrrev_b16_e32 v181, 11, v50
	v_lshrrev_b16_e32 v186, 13, v111
	v_lshlrev_b16_e32 v50, 4, v181
	v_lshlrev_b16_e32 v111, 4, v186
	v_add_u16_e32 v50, v119, v50
	v_add_u16_e32 v111, v119, v111
	v_ashrrev_i32_e32 v110, 6, v175
	v_lshlrev_b16_e32 v50, 2, v50
	v_lshlrev_b16_e32 v111, 2, v111
	v_cmp_lt_u32_e32 vcc, 47, v119
	v_lshlrev_b32_e32 v108, 2, v118
	v_mov_b32_e32 v55, v109
	v_and_b32_e32 v142, 0xfc, v50
	v_and_b32_e32 v138, 0xfc, v111
	v_lshlrev_b32_e32 v194, 4, v110
	v_cndmask_b32_e64 v192, 0, 1, vcc
	v_lshl_add_u64 v[56:57], s[50:51], 0, v[108:109]
	v_lshlrev_b64 v[116:117], 2, v[54:55]
	v_lshlrev_b32_e32 v114, 2, v142
	v_mov_b32_e32 v115, v109
	v_lshlrev_b32_e32 v112, 2, v138
	v_mov_b32_e32 v113, v109
	v_or_b32_e32 v176, v194, v192
	v_lshl_add_u64 v[52:53], v[56:57], 0, v[116:117]
	v_lshl_add_u64 v[50:51], v[56:57], 0, v[114:115]
	v_lshl_add_u64 v[162:163], v[56:57], 0, v[112:113]
	v_mul_lo_u32 v56, v176, s67
	v_lshlrev_b32_e32 v57, 2, v54
	s_movk_i32 s2, 0xff
	v_add3_u32 v178, 0, v56, v57
	v_bitop3_b16 v56, v175, s2, v169 bitop3:0xc8
	v_mul_lo_u16_e32 v56, 0xab, v56
	v_lshrrev_b16_e32 v191, 13, v56
	v_mul_lo_u16_e32 v56, 48, v191
	v_sub_u16_e32 v56, v175, v56
	v_lshlrev_b16_e32 v203, 2, v56
	v_or_b32_e32 v56, 0x100, v119
	s_movk_i32 s2, 0x556
	v_mul_u32_u24_sdwa v190, v56, s2 dst_sel:DWORD dst_unused:UNUSED_PAD src0_sel:WORD_0 src1_sel:DWORD
	v_mul_lo_u16_sdwa v57, v190, v170 dst_sel:DWORD dst_unused:UNUSED_PAD src0_sel:WORD_1 src1_sel:DWORD
	v_sub_u16_e32 v56, v56, v57
	v_lshlrev_b16_e32 v202, 2, v56
	v_or_b32_e32 v56, 0x140, v119
	v_mul_u32_u24_sdwa v189, v56, s2 dst_sel:DWORD dst_unused:UNUSED_PAD src0_sel:WORD_0 src1_sel:DWORD
	v_mul_lo_u16_sdwa v57, v189, v170 dst_sel:DWORD dst_unused:UNUSED_PAD src0_sel:WORD_1 src1_sel:DWORD
	v_sub_u16_e32 v56, v56, v57
	v_lshlrev_b16_e32 v201, 2, v56
	v_or_b32_e32 v56, 0x180, v119
	v_mul_u32_u24_sdwa v188, v56, s2 dst_sel:DWORD dst_unused:UNUSED_PAD src0_sel:WORD_0 src1_sel:DWORD
	v_mul_lo_u16_sdwa v57, v188, v170 dst_sel:DWORD dst_unused:UNUSED_PAD src0_sel:WORD_1 src1_sel:DWORD
	v_sub_u16_e32 v56, v56, v57
	v_lshlrev_b16_e32 v200, 2, v56
	v_or_b32_e32 v56, 0x1c0, v119
	v_mul_u32_u24_sdwa v187, v56, s2 dst_sel:DWORD dst_unused:UNUSED_PAD src0_sel:WORD_0 src1_sel:DWORD
	v_mul_lo_u16_sdwa v57, v187, v170 dst_sel:DWORD dst_unused:UNUSED_PAD src0_sel:WORD_1 src1_sel:DWORD
	v_sub_u16_e32 v56, v56, v57
	v_lshlrev_b16_e32 v199, 2, v56
	v_or_b32_e32 v56, 0x200, v119
	v_mul_u32_u24_sdwa v185, v56, s2 dst_sel:DWORD dst_unused:UNUSED_PAD src0_sel:WORD_0 src1_sel:DWORD
	v_mul_lo_u16_sdwa v57, v185, v170 dst_sel:DWORD dst_unused:UNUSED_PAD src0_sel:WORD_1 src1_sel:DWORD
	v_sub_u16_e32 v56, v56, v57
	v_lshlrev_b16_e32 v198, 2, v56
	v_or_b32_e32 v56, 0x240, v119
	v_mul_u32_u24_sdwa v184, v56, s2 dst_sel:DWORD dst_unused:UNUSED_PAD src0_sel:WORD_0 src1_sel:DWORD
	v_mul_lo_u16_sdwa v57, v184, v170 dst_sel:DWORD dst_unused:UNUSED_PAD src0_sel:WORD_1 src1_sel:DWORD
	v_sub_u16_e32 v56, v56, v57
	v_lshlrev_b16_e32 v197, 2, v56
	v_or_b32_e32 v56, 0x280, v119
	v_mul_u32_u24_sdwa v182, v56, s2 dst_sel:DWORD dst_unused:UNUSED_PAD src0_sel:WORD_0 src1_sel:DWORD
	v_mul_lo_u16_sdwa v57, v182, v170 dst_sel:DWORD dst_unused:UNUSED_PAD src0_sel:WORD_1 src1_sel:DWORD
	v_sub_u16_e32 v56, v56, v57
	v_lshl_add_u64 v[110:111], s[46:47], 0, v[108:109]
	v_lshlrev_b16_e32 v196, 2, v56
	v_or_b32_e32 v56, 0x2c0, v119
	v_lshlrev_b32_e32 v108, 1, v118
	v_add_u32_e32 v193, v194, v174
	v_mul_u32_u24_sdwa v183, v56, s2 dst_sel:DWORD dst_unused:UNUSED_PAD src0_sel:WORD_0 src1_sel:DWORD
	v_lshl_add_u64 v[118:119], s[38:39], 0, v[108:109]
	v_or_b32_sdwa v120, v193, v182 dst_sel:DWORD dst_unused:UNUSED_PAD src0_sel:DWORD src1_sel:WORD_1
	v_mul_lo_u16_sdwa v57, v183, v170 dst_sel:DWORD dst_unused:UNUSED_PAD src0_sel:WORD_1 src1_sel:DWORD
	v_mad_i64_i32 v[122:123], s[2:3], v120, s56, v[118:119]
	v_lshlrev_b32_e32 v120, 1, v196
	v_mov_b32_e32 v121, v109
	v_sub_u16_e32 v56, v56, v57
	v_lshl_add_u64 v[128:129], v[122:123], 0, v[120:121]
	v_or_b32_sdwa v122, v193, v184 dst_sel:DWORD dst_unused:UNUSED_PAD src0_sel:DWORD src1_sel:WORD_1
	v_lshlrev_b16_e32 v195, 2, v56
	v_or_b32_sdwa v56, v193, v183 dst_sel:DWORD dst_unused:UNUSED_PAD src0_sel:DWORD src1_sel:WORD_1
	v_mad_i64_i32 v[124:125], s[2:3], v122, s56, v[118:119]
	v_lshlrev_b32_e32 v122, 1, v197
	v_mov_b32_e32 v123, v109
	v_mad_i64_i32 v[56:57], s[2:3], v56, s56, v[118:119]
	v_lshlrev_b32_e32 v108, 1, v195
	v_lshl_add_u64 v[130:131], v[124:125], 0, v[122:123]
	v_or_b32_sdwa v124, v193, v185 dst_sel:DWORD dst_unused:UNUSED_PAD src0_sel:DWORD src1_sel:WORD_1
	v_lshl_add_u64 v[56:57], v[56:57], 0, v[108:109]
	v_mad_i64_i32 v[126:127], s[2:3], v124, s56, v[118:119]
	v_lshlrev_b32_e32 v124, 1, v198
	v_mov_b32_e32 v125, v109
	s_waitcnt vmcnt(0)
	s_barrier
	s_mov_b64 s[10:11], 0x30000
	v_lshl_add_u64 v[132:133], v[126:127], 0, v[124:125]
	v_lshl_add_u64 v[254:255], v[56:57], 0, s[10:11]
	global_load_dwordx2 v[126:127], v[56:57], off nt
	v_lshl_add_u64 v[252:253], v[128:129], 0, s[10:11]
	global_load_dwordx2 v[136:137], v[128:129], off nt
	v_lshl_add_u64 v[250:251], v[130:131], 0, s[10:11]
	global_load_dwordx2 v[146:147], v[130:131], off nt
	v_lshl_add_u64 v[248:249], v[132:133], 0, s[10:11]
	global_load_dwordx2 v[148:149], v[132:133], off nt
	v_or_b32_e32 v128, v193, v191
	v_and_b32_e32 v204, 0xfc, v203
	v_mad_i64_i32 v[130:131], s[2:3], v128, s56, v[118:119]
	v_lshlrev_b32_e32 v128, 1, v204
	v_mov_b32_e32 v129, v109
	v_lshl_add_u64 v[134:135], v[130:131], 0, v[128:129]
	v_or_b32_e32 v130, v193, v186
	v_mad_i64_i32 v[132:133], s[2:3], v130, s56, v[118:119]
	v_lshlrev_b32_e32 v130, 1, v138
	v_mov_b32_e32 v131, v109
	v_lshl_add_u64 v[138:139], v[132:133], 0, v[130:131]
	v_or_b32_e32 v132, v193, v181
	v_mad_i64_i32 v[140:141], s[2:3], v132, s56, v[118:119]
	v_lshlrev_b32_e32 v132, 1, v142
	v_mov_b32_e32 v133, v109
	v_or_b32_e32 v142, v193, v192
	v_lshl_add_u64 v[140:141], v[140:141], 0, v[132:133]
	v_mad_i64_i32 v[144:145], s[2:3], v142, s56, v[118:119]
	v_lshlrev_b64 v[142:143], 1, v[54:55]
	v_or_b32_sdwa v56, v193, v187 dst_sel:DWORD dst_unused:UNUSED_PAD src0_sel:DWORD src1_sel:WORD_1
	v_lshl_add_u64 v[54:55], v[144:145], 0, v[142:143]
	v_lshl_add_u64 v[238:239], v[134:135], 0, s[10:11]
	global_load_dwordx2 v[158:159], v[134:135], off nt
	v_lshl_add_u64 v[236:237], v[138:139], 0, s[10:11]
	global_load_dwordx2 v[160:161], v[138:139], off nt
	v_lshl_add_u64 v[234:235], v[140:141], 0, s[10:11]
	global_load_dwordx2 v[164:165], v[140:141], off nt
	v_lshl_add_u64 v[232:233], v[54:55], 0, s[10:11]
	global_load_dwordx2 v[166:167], v[54:55], off nt
	v_or_b32_sdwa v140, v193, v189 dst_sel:DWORD dst_unused:UNUSED_PAD src0_sel:DWORD src1_sel:WORD_1
	v_mad_i64_i32 v[56:57], s[2:3], v56, s56, v[118:119]
	v_lshlrev_b32_e32 v134, 1, v199
	v_mov_b32_e32 v135, v109
	v_mad_i64_i32 v[144:145], s[2:3], v140, s56, v[118:119]
	v_lshlrev_b32_e32 v140, 1, v201
	v_mov_b32_e32 v141, v109
	v_lshl_add_u64 v[54:55], v[56:57], 0, v[134:135]
	v_or_b32_sdwa v56, v193, v188 dst_sel:DWORD dst_unused:UNUSED_PAD src0_sel:DWORD src1_sel:WORD_1
	v_lshl_add_u64 v[154:155], v[144:145], 0, v[140:141]
	v_or_b32_sdwa v144, v193, v190 dst_sel:DWORD dst_unused:UNUSED_PAD src0_sel:DWORD src1_sel:WORD_1
	v_mad_i64_i32 v[56:57], s[2:3], v56, s56, v[118:119]
	v_lshlrev_b32_e32 v138, 1, v200
	v_mov_b32_e32 v139, v109
	v_mad_i64_i32 v[150:151], s[2:3], v144, s56, v[118:119]
	v_lshlrev_b32_e32 v144, 1, v202
	v_mov_b32_e32 v145, v109
	v_lshl_add_u64 v[56:57], v[56:57], 0, v[138:139]
	v_lshl_add_u64 v[156:157], v[150:151], 0, v[144:145]
	v_lshl_add_u64 v[246:247], v[54:55], 0, s[10:11]
	global_load_dwordx2 v[150:151], v[54:55], off nt
	v_lshl_add_u64 v[244:245], v[56:57], 0, s[10:11]
	global_load_dwordx2 v[152:153], v[56:57], off nt
	s_nop 0
	v_lshl_add_u64 v[242:243], v[154:155], 0, s[10:11]
	global_load_dwordx2 v[154:155], v[154:155], off nt
	s_nop 0
	v_lshl_add_u64 v[240:241], v[156:157], 0, s[10:11]
	global_load_dwordx2 v[156:157], v[156:157], off nt
	v_and_b32_e32 v205, 16, v175
	v_lshrrev_b32_e32 v207, 2, v175
	global_load_dwordx4 v[54:57], v[52:53], off
	v_or_b32_e32 v206, v179, v177
	v_and_or_b32 v180, v207, 12, v180
	v_bitop3_b32 v177, v179, v205, v177 bitop3:0x36
	global_load_dwordx4 v[50:53], v[50:51], off
	v_lshlrev_b32_e32 v177, 2, v177
	v_mul_lo_u32 v179, v180, s67
	v_add3_u32 v177, 0, v177, v179
	ds_write2st64_b32 v177, v58, v59 offset1:3
	ds_write2st64_b32 v177, v60, v61 offset0:6 offset1:9
	ds_write2st64_b32 v177, v102, v103 offset0:48 offset1:51
	ds_write2st64_b32 v177, v104, v105 offset0:54 offset1:57
	v_add_u32_e32 v58, 16, v206
	v_bitop3_b32 v58, v58, v175, 16 bitop3:0x78
	v_lshlrev_b32_e32 v58, 2, v58
	v_add3_u32 v102, 0, v58, v179
	global_load_dwordx4 v[58:61], v[162:163], off
	global_load_dwordx2 v[232:233], v[232:233], off nt
	global_load_dwordx2 v[234:235], v[234:235], off nt
	global_load_dwordx2 v[236:237], v[236:237], off nt
	global_load_dwordx2 v[238:239], v[238:239], off nt
	global_load_dwordx2 v[240:241], v[240:241], off nt
	global_load_dwordx2 v[242:243], v[242:243], off nt
	global_load_dwordx2 v[244:245], v[244:245], off nt
	global_load_dwordx2 v[246:247], v[246:247], off nt
	global_load_dwordx2 v[248:249], v[248:249], off nt
	global_load_dwordx2 v[250:251], v[250:251], off nt
	global_load_dwordx2 v[252:253], v[252:253], off nt
	global_load_dwordx2 v[254:255], v[254:255], off nt
	ds_write2st64_b32 v102, v78, v79 offset1:3
	v_add_u32_e32 v78, 32, v206
	v_bitop3_b32 v78, v78, v175, 16 bitop3:0x78
	v_lshlrev_b32_e32 v78, 2, v78
	v_add3_u32 v103, 0, v78, v179
	ds_write2st64_b32 v102, v80, v81 offset0:6 offset1:9
	ds_write2st64_b32 v102, v86, v87 offset0:48 offset1:51
	ds_write2st64_b32 v102, v88, v89 offset0:54 offset1:57
	ds_write2st64_b32 v103, v62, v63 offset1:3
	ds_write2st64_b32 v103, v64, v65 offset0:6 offset1:9
	ds_write2st64_b32 v103, v70, v71 offset0:48 offset1:51
	ds_write2st64_b32 v103, v72, v73 offset0:54 offset1:57
	v_add_u32_e32 v62, 0x60, v206
	v_bitop3_b32 v62, v62, v175, 16 bitop3:0x78
	v_lshlrev_b32_e32 v62, 2, v62
	v_add3_u32 v104, 0, v62, v179
	v_add_u32_e32 v62, 0x70, v206
	v_bitop3_b32 v62, v62, v175, 16 bitop3:0x78
	v_lshlrev_b32_e32 v62, 2, v62
	s_movk_i32 s2, 0x80
	ds_write2st64_b32 v104, v94, v95 offset1:3
	ds_write2st64_b32 v104, v96, v97 offset0:6 offset1:9
	ds_write2st64_b32 v104, v98, v99 offset0:48 offset1:51
	ds_write2st64_b32 v104, v100, v101 offset0:54 offset1:57
	v_add3_u32 v101, 0, v62, v179
	v_bitop3_b32 v62, v206, v205, s2 bitop3:0x36
	v_lshlrev_b32_e32 v62, 2, v62
	v_add3_u32 v105, 0, v62, v179
	v_add_u32_e32 v62, v176, v174
	v_mad_i64_i32 v[62:63], s[2:3], v62, s62, v[110:111]
	v_or_b32_e32 v99, v194, v181
	ds_write2st64_b32 v101, v82, v83 offset1:3
	ds_write2st64_b32 v101, v84, v85 offset0:6 offset1:9
	ds_write2st64_b32 v101, v90, v91 offset0:48 offset1:51
	ds_write2st64_b32 v101, v92, v93 offset0:54 offset1:57
	ds_write2st64_b32 v105, v66, v67 offset1:3
	ds_write2st64_b32 v105, v68, v69 offset0:6 offset1:9
	ds_write2st64_b32 v105, v74, v75 offset0:48 offset1:51
	ds_write2st64_b32 v105, v76, v77 offset0:54 offset1:57
	v_lshl_add_u64 v[74:75], v[62:63], 0, v[116:117]
	v_mul_lo_u32 v62, v99, s67
	v_add3_u32 v100, 0, v62, v114
	v_add_u32_e32 v62, v99, v174
	v_mad_i64_i32 v[62:63], s[2:3], v62, s62, v[110:111]
	v_or_b32_e32 v98, v194, v186
	v_lshl_add_u64 v[80:81], v[62:63], 0, v[114:115]
	v_mul_lo_u32 v66, v98, s67
	s_waitcnt lgkmcnt(0)
	s_barrier
	ds_read_b128 v[62:65], v178
	s_waitcnt vmcnt(19)
	v_cvt_f32_f16_e32 v70, v166
	v_cvt_f32_f16_sdwa v71, v166 dst_sel:DWORD dst_unused:UNUSED_PAD src0_sel:WORD_1
	v_cvt_f32_f16_e32 v72, v167
	v_cvt_f32_f16_sdwa v73, v167 dst_sel:DWORD dst_unused:UNUSED_PAD src0_sel:WORD_1
	v_add3_u32 v162, 0, v66, v112
	ds_read_b128 v[66:69], v100
	v_cvt_f32_f16_e32 v76, v164
	v_cvt_f32_f16_sdwa v77, v164 dst_sel:DWORD dst_unused:UNUSED_PAD src0_sel:WORD_1
	v_cvt_f32_f16_e32 v78, v165
	v_cvt_f32_f16_sdwa v79, v165 dst_sel:DWORD dst_unused:UNUSED_PAD src0_sel:WORD_1
	v_cvt_f32_f16_e32 v82, v160
	v_cvt_f32_f16_sdwa v83, v160 dst_sel:DWORD dst_unused:UNUSED_PAD src0_sel:WORD_1
	v_or_b32_e32 v160, v194, v191
	v_cvt_f32_f16_e32 v86, v147
	v_cvt_f32_f16_sdwa v87, v147 dst_sel:DWORD dst_unused:UNUSED_PAD src0_sel:WORD_1
	v_cvt_f32_f16_e32 v88, v126
	v_cvt_f32_f16_e32 v90, v127
	v_cvt_f32_f16_sdwa v91, v127 dst_sel:DWORD dst_unused:UNUSED_PAD src0_sel:WORD_1
	v_cvt_f32_f16_sdwa v89, v126 dst_sel:DWORD dst_unused:UNUSED_PAD src0_sel:WORD_1
	v_add_u32_e32 v163, 0x80, v193
	s_waitcnt vmcnt(18)
	v_cvt_f32_f16_e32 v84, v151
	v_cvt_f32_f16_sdwa v85, v151 dst_sel:DWORD dst_unused:UNUSED_PAD src0_sel:WORD_1
	s_waitcnt vmcnt(14) lgkmcnt(1)
	v_pk_fma_f32 v[64:65], v[72:73], v[56:57], v[64:65]
	v_pk_fma_f32 v[62:63], v[70:71], v[54:55], v[62:63]
	global_store_dwordx4 v[74:75], v[62:65], off nt
	v_cvt_f32_f16_e32 v70, v161
	v_cvt_f32_f16_sdwa v71, v161 dst_sel:DWORD dst_unused:UNUSED_PAD src0_sel:WORD_1
	s_waitcnt vmcnt(14) lgkmcnt(0)
	v_pk_fma_f32 v[64:65], v[78:79], v[52:53], v[68:69]
	v_pk_fma_f32 v[62:63], v[76:77], v[50:51], v[66:67]
	v_xor_b32_e32 v67, 16, v203
	global_store_dwordx4 v[80:81], v[62:65], off nt
	ds_read_b128 v[62:65], v162
	v_and_b32_e32 v67, 0xfc, v67
	v_mul_lo_u32 v66, v160, s67
	v_lshlrev_b32_e32 v67, 2, v67
	v_add3_u32 v161, 0, v66, v67
	ds_read_b128 v[66:69], v161
	v_cvt_f32_f16_e32 v72, v158
	v_cvt_f32_f16_sdwa v73, v158 dst_sel:DWORD dst_unused:UNUSED_PAD src0_sel:WORD_1
	s_waitcnt vmcnt(14) lgkmcnt(1)
	v_pk_fma_f32 v[64:65], v[70:71], v[60:61], v[64:65]
	v_add_u32_e32 v70, v98, v174
	v_mad_i64_i32 v[70:71], s[2:3], v70, s62, v[110:111]
	v_cvt_f32_f16_e32 v74, v159
	v_cvt_f32_f16_sdwa v75, v159 dst_sel:DWORD dst_unused:UNUSED_PAD src0_sel:WORD_1
	v_pk_fma_f32 v[62:63], v[82:83], v[58:59], v[62:63]
	v_lshl_add_u64 v[70:71], v[70:71], 0, v[112:113]
	global_store_dwordx4 v[70:71], v[62:65], off nt
	v_lshlrev_b32_e32 v70, 2, v204
	v_mov_b32_e32 v71, v109
	s_waitcnt lgkmcnt(0)
	v_pk_fma_f32 v[62:63], v[72:73], v[54:55], v[66:67]
	v_add_u32_e32 v66, v160, v174
	v_mad_i64_i32 v[66:67], s[2:3], v66, s62, v[110:111]
	v_pk_fma_f32 v[64:65], v[74:75], v[56:57], v[68:69]
	v_lshl_add_u64 v[66:67], v[66:67], 0, v[70:71]
	global_store_dwordx4 v[66:67], v[62:65], off nt
	v_or_b32_sdwa v158, v194, v190 dst_sel:DWORD dst_unused:UNUSED_PAD src0_sel:DWORD src1_sel:WORD_1
	v_cvt_f32_f16_e32 v66, v156
	v_xor_b32_e32 v63, 16, v202
	v_mul_lo_u32 v62, v158, s67
	v_lshlrev_b32_sdwa v63, v171, v63 dst_sel:DWORD dst_unused:UNUSED_PAD src0_sel:DWORD src1_sel:WORD_0
	v_add3_u32 v159, 0, v62, v63
	ds_read_b128 v[62:65], v159
	v_cvt_f32_f16_sdwa v67, v156 dst_sel:DWORD dst_unused:UNUSED_PAD src0_sel:WORD_1
	v_or_b32_sdwa v156, v194, v189 dst_sel:DWORD dst_unused:UNUSED_PAD src0_sel:DWORD src1_sel:WORD_1
	v_xor_b32_e32 v73, 16, v201
	v_cvt_f32_f16_e32 v68, v157
	v_cvt_f32_f16_sdwa v69, v157 dst_sel:DWORD dst_unused:UNUSED_PAD src0_sel:WORD_1
	v_mul_lo_u32 v72, v156, s67
	v_lshlrev_b32_sdwa v73, v171, v73 dst_sel:DWORD dst_unused:UNUSED_PAD src0_sel:DWORD src1_sel:WORD_0
	v_add3_u32 v157, 0, v72, v73
	ds_read_b128 v[72:75], v157
	s_waitcnt lgkmcnt(1)
	v_pk_fma_f32 v[62:63], v[66:67], v[50:51], v[62:63]
	v_add_u32_e32 v66, v158, v174
	v_cvt_f32_f16_e32 v76, v154
	v_cvt_f32_f16_sdwa v77, v154 dst_sel:DWORD dst_unused:UNUSED_PAD src0_sel:WORD_1
	v_pk_fma_f32 v[64:65], v[68:69], v[52:53], v[64:65]
	v_mad_i64_i32 v[66:67], s[2:3], v66, s62, v[110:111]
	v_lshlrev_b32_e32 v68, 2, v202
	v_mov_b32_e32 v69, v109
	v_cvt_f32_f16_e32 v78, v155
	v_cvt_f32_f16_sdwa v79, v155 dst_sel:DWORD dst_unused:UNUSED_PAD src0_sel:WORD_1
	v_lshl_add_u64 v[66:67], v[66:67], 0, v[68:69]
	global_store_dwordx4 v[66:67], v[62:65], off nt
	v_add_u32_e32 v66, v156, v174
	v_mad_i64_i32 v[66:67], s[2:3], v66, s62, v[110:111]
	s_waitcnt lgkmcnt(0)
	v_pk_fma_f32 v[62:63], v[76:77], v[58:59], v[72:73]
	v_lshlrev_b32_e32 v72, 2, v201
	v_mov_b32_e32 v73, v109
	v_pk_fma_f32 v[64:65], v[78:79], v[60:61], v[74:75]
	v_lshl_add_u64 v[66:67], v[66:67], 0, v[72:73]
	v_or_b32_sdwa v154, v194, v188 dst_sel:DWORD dst_unused:UNUSED_PAD src0_sel:DWORD src1_sel:WORD_1
	global_store_dwordx4 v[66:67], v[62:65], off nt
	v_cvt_f32_f16_e32 v82, v153
	v_cvt_f32_f16_sdwa v83, v153 dst_sel:DWORD dst_unused:UNUSED_PAD src0_sel:WORD_1
	v_mul_lo_u32 v63, v154, s67
	v_lshlrev_b32_e32 v62, 2, v200
	v_add3_u32 v155, 0, v63, v62
	ds_read_b128 v[74:77], v155
	v_cvt_f32_f16_e32 v64, v152
	v_cvt_f32_f16_sdwa v65, v152 dst_sel:DWORD dst_unused:UNUSED_PAD src0_sel:WORD_1
	v_or_b32_sdwa v152, v194, v187 dst_sel:DWORD dst_unused:UNUSED_PAD src0_sel:DWORD src1_sel:WORD_1
	v_mul_lo_u32 v63, v152, s67
	v_lshlrev_b32_e32 v66, 2, v199
	v_add3_u32 v153, 0, v63, v66
	ds_read_b128 v[78:81], v153
	v_add_u32_e32 v63, v154, v174
	s_waitcnt lgkmcnt(1)
	v_pk_fma_f32 v[76:77], v[82:83], v[56:57], v[76:77]
	v_pk_fma_f32 v[74:75], v[64:65], v[54:55], v[74:75]
	v_mad_i64_i32 v[64:65], s[2:3], v63, s62, v[110:111]
	v_mov_b32_e32 v63, v109
	v_cvt_f32_f16_e32 v82, v150
	v_cvt_f32_f16_sdwa v83, v150 dst_sel:DWORD dst_unused:UNUSED_PAD src0_sel:WORD_1
	v_lshl_add_u64 v[64:65], v[64:65], 0, v[62:63]
	global_store_dwordx4 v[64:65], v[74:77], off nt
	v_add_u32_e32 v64, v152, v174
	v_mad_i64_i32 v[64:65], s[2:3], v64, s62, v[110:111]
	v_mov_b32_e32 v67, v109
	s_waitcnt lgkmcnt(0)
	v_pk_fma_f32 v[76:77], v[84:85], v[52:53], v[80:81]
	v_pk_fma_f32 v[74:75], v[82:83], v[50:51], v[78:79]
	v_lshl_add_u64 v[64:65], v[64:65], 0, v[66:67]
	v_or_b32_sdwa v150, v194, v185 dst_sel:DWORD dst_unused:UNUSED_PAD src0_sel:DWORD src1_sel:WORD_1
	global_store_dwordx4 v[64:65], v[74:77], off nt
	v_mul_lo_u32 v65, v150, s67
	v_lshlrev_b32_e32 v64, 2, v198
	v_add3_u32 v151, 0, v65, v64
	ds_read_b128 v[74:77], v151
	v_cvt_f32_f16_e32 v82, v148
	v_cvt_f32_f16_sdwa v83, v148 dst_sel:DWORD dst_unused:UNUSED_PAD src0_sel:WORD_1
	v_cvt_f32_f16_e32 v84, v149
	v_cvt_f32_f16_sdwa v85, v149 dst_sel:DWORD dst_unused:UNUSED_PAD src0_sel:WORD_1
	v_or_b32_sdwa v148, v194, v184 dst_sel:DWORD dst_unused:UNUSED_PAD src0_sel:DWORD src1_sel:WORD_1
	v_xor_b32_e32 v78, 16, v197
	v_mul_lo_u32 v65, v148, s67
	v_lshlrev_b32_sdwa v78, v171, v78 dst_sel:DWORD dst_unused:UNUSED_PAD src0_sel:DWORD src1_sel:WORD_0
	v_add3_u32 v149, 0, v65, v78
	ds_read_b128 v[78:81], v149
	v_add_u32_e32 v65, v150, v174
	s_waitcnt lgkmcnt(1)
	v_pk_fma_f32 v[76:77], v[84:85], v[60:61], v[76:77]
	v_pk_fma_f32 v[74:75], v[82:83], v[58:59], v[74:75]
	v_mad_i64_i32 v[82:83], s[2:3], v65, s62, v[110:111]
	v_mov_b32_e32 v65, v109
	v_cvt_f32_f16_e32 v84, v146
	v_cvt_f32_f16_sdwa v85, v146 dst_sel:DWORD dst_unused:UNUSED_PAD src0_sel:WORD_1
	v_lshl_add_u64 v[82:83], v[82:83], 0, v[64:65]
	global_store_dwordx4 v[82:83], v[74:77], off nt
	s_waitcnt lgkmcnt(0)
	v_pk_fma_f32 v[80:81], v[86:87], v[56:57], v[80:81]
	v_pk_fma_f32 v[78:79], v[84:85], v[54:55], v[78:79]
	v_add_u32_e32 v74, v148, v174
	v_mad_i64_i32 v[74:75], s[2:3], v74, s62, v[110:111]
	v_lshlrev_b32_e32 v76, 2, v197
	v_mov_b32_e32 v77, v109
	v_lshl_add_u64 v[74:75], v[74:75], 0, v[76:77]
	global_store_dwordx4 v[74:75], v[78:81], off nt
	v_or_b32_sdwa v146, v194, v182 dst_sel:DWORD dst_unused:UNUSED_PAD src0_sel:DWORD src1_sel:WORD_1
	v_xor_b32_e32 v75, 16, v196
	v_mul_lo_u32 v74, v146, s67
	v_lshlrev_b32_sdwa v75, v171, v75 dst_sel:DWORD dst_unused:UNUSED_PAD src0_sel:DWORD src1_sel:WORD_0
	v_add3_u32 v147, 0, v74, v75
	ds_read_b128 v[78:81], v147
	v_cvt_f32_f16_e32 v74, v136
	v_cvt_f32_f16_sdwa v75, v136 dst_sel:DWORD dst_unused:UNUSED_PAD src0_sel:WORD_1
	v_cvt_f32_f16_e32 v86, v137
	v_cvt_f32_f16_sdwa v87, v137 dst_sel:DWORD dst_unused:UNUSED_PAD src0_sel:WORD_1
	v_or_b32_sdwa v136, v194, v183 dst_sel:DWORD dst_unused:UNUSED_PAD src0_sel:DWORD src1_sel:WORD_1
	v_xor_b32_e32 v83, 16, v195
	v_mul_lo_u32 v82, v136, s67
	v_lshlrev_b32_sdwa v83, v171, v83 dst_sel:DWORD dst_unused:UNUSED_PAD src0_sel:DWORD src1_sel:WORD_0
	v_add3_u32 v137, 0, v82, v83
	ds_read_b128 v[82:85], v137
	s_waitcnt lgkmcnt(1)
	v_pk_fma_f32 v[78:79], v[74:75], v[50:51], v[78:79]
	v_add_u32_e32 v74, v146, v174
	v_pk_fma_f32 v[80:81], v[86:87], v[52:53], v[80:81]
	v_mad_i64_i32 v[86:87], s[2:3], v74, s62, v[110:111]
	v_lshlrev_b32_e32 v74, 2, v196
	v_mov_b32_e32 v75, v109
	v_lshl_add_u64 v[86:87], v[86:87], 0, v[74:75]
	global_store_dwordx4 v[86:87], v[78:81], off nt
	s_waitcnt lgkmcnt(0)
	v_pk_fma_f32 v[84:85], v[90:91], v[60:61], v[84:85]
	v_pk_fma_f32 v[82:83], v[88:89], v[58:59], v[82:83]
	v_add_u32_e32 v78, v136, v174
	v_mad_i64_i32 v[80:81], s[2:3], v78, s62, v[110:111]
	v_lshlrev_b32_e32 v78, 2, v195
	v_mov_b32_e32 v79, v109
	v_lshl_add_u64 v[80:81], v[80:81], 0, v[78:79]
	global_store_dwordx4 v[80:81], v[82:85], off nt
	v_or_b32_e32 v80, v163, v192
	v_mad_i64_i32 v[80:81], s[2:3], v80, s56, v[118:119]
	v_lshl_add_u64 v[80:81], v[80:81], 0, v[142:143]
	v_or_b32_e32 v80, v163, v181
	v_mad_i64_i32 v[80:81], s[2:3], v80, s56, v[118:119]
	v_or_b32_e32 v82, v163, v186
	v_or_b32_e32 v84, v163, v191
	v_lshl_add_u64 v[80:81], v[80:81], 0, v[132:133]
	v_mad_i64_i32 v[82:83], s[2:3], v82, s56, v[118:119]
	v_mad_i64_i32 v[84:85], s[2:3], v84, s56, v[118:119]
	v_lshl_add_u64 v[82:83], v[82:83], 0, v[130:131]
	v_lshl_add_u64 v[84:85], v[84:85], 0, v[128:129]
	v_or_b32_sdwa v80, v163, v190 dst_sel:DWORD dst_unused:UNUSED_PAD src0_sel:DWORD src1_sel:WORD_1
	v_mad_i64_i32 v[80:81], s[2:3], v80, s56, v[118:119]
	v_or_b32_sdwa v82, v163, v189 dst_sel:DWORD dst_unused:UNUSED_PAD src0_sel:DWORD src1_sel:WORD_1
	v_or_b32_sdwa v84, v163, v188 dst_sel:DWORD dst_unused:UNUSED_PAD src0_sel:DWORD src1_sel:WORD_1
	v_or_b32_sdwa v86, v163, v187 dst_sel:DWORD dst_unused:UNUSED_PAD src0_sel:DWORD src1_sel:WORD_1
	v_lshl_add_u64 v[80:81], v[80:81], 0, v[144:145]
	v_mad_i64_i32 v[82:83], s[2:3], v82, s56, v[118:119]
	v_mad_i64_i32 v[84:85], s[2:3], v84, s56, v[118:119]
	v_mad_i64_i32 v[86:87], s[2:3], v86, s56, v[118:119]
	v_lshl_add_u64 v[82:83], v[82:83], 0, v[140:141]
	v_lshl_add_u64 v[84:85], v[84:85], 0, v[138:139]
	v_lshl_add_u64 v[86:87], v[86:87], 0, v[134:135]
	v_or_b32_sdwa v84, v163, v182 dst_sel:DWORD dst_unused:UNUSED_PAD src0_sel:DWORD src1_sel:WORD_1
	v_or_b32_sdwa v80, v163, v185 dst_sel:DWORD dst_unused:UNUSED_PAD src0_sel:DWORD src1_sel:WORD_1
	v_or_b32_sdwa v82, v163, v184 dst_sel:DWORD dst_unused:UNUSED_PAD src0_sel:DWORD src1_sel:WORD_1
	v_mad_i64_i32 v[84:85], s[2:3], v84, s56, v[118:119]
	v_mad_i64_i32 v[80:81], s[2:3], v80, s56, v[118:119]
	v_mad_i64_i32 v[82:83], s[2:3], v82, s56, v[118:119]
	v_lshl_add_u64 v[120:121], v[84:85], 0, v[120:121]
	v_or_b32_sdwa v84, v163, v183 dst_sel:DWORD dst_unused:UNUSED_PAD src0_sel:DWORD src1_sel:WORD_1
	v_lshl_add_u64 v[80:81], v[80:81], 0, v[124:125]
	v_lshl_add_u64 v[82:83], v[82:83], 0, v[122:123]
	v_mad_i64_i32 v[84:85], s[2:3], v84, s56, v[118:119]
	v_lshl_add_u64 v[118:119], v[84:85], 0, v[108:109]
	s_nop 0
	s_barrier
	ds_write2st64_b32 v177, v14, v15 offset1:3
	ds_write2st64_b32 v177, v16, v17 offset0:6 offset1:9
	ds_write2st64_b32 v177, v38, v39 offset0:48 offset1:51
	ds_write2st64_b32 v177, v40, v41 offset0:54 offset1:57
	ds_write2st64_b32 v102, v6, v7 offset1:3
	ds_write2st64_b32 v102, v8, v9 offset0:6 offset1:9
	ds_write2st64_b32 v102, v26, v27 offset0:48 offset1:51
	ds_write2st64_b32 v102, v28, v29 offset0:54 offset1:57
	ds_write2st64_b32 v103, v2, v3 offset1:3
	ds_write2st64_b32 v103, v4, v5 offset0:6 offset1:9
	ds_write2st64_b32 v103, v18, v19 offset0:48 offset1:51
	ds_write2st64_b32 v103, v20, v21 offset0:54 offset1:57
	ds_write2st64_b32 v104, v30, v31 offset1:3
	ds_write2st64_b32 v104, v32, v33 offset0:6 offset1:9
	ds_write2st64_b32 v104, v46, v47 offset0:48 offset1:51
	ds_write2st64_b32 v104, v48, v49 offset0:54 offset1:57
	ds_write2st64_b32 v101, v22, v23 offset1:3
	ds_write2st64_b32 v101, v24, v25 offset0:6 offset1:9
	ds_write2st64_b32 v101, v42, v43 offset0:48 offset1:51
	ds_write2st64_b32 v101, v44, v45 offset0:54 offset1:57
	ds_write2st64_b32 v105, v10, v11 offset1:3
	ds_write2st64_b32 v105, v12, v13 offset0:6 offset1:9
	ds_write2st64_b32 v105, v34, v35 offset0:48 offset1:51
	ds_write2st64_b32 v105, v36, v37 offset0:54 offset1:57
	s_waitcnt lgkmcnt(0)
	s_barrier
	s_and_saveexec_b64 s[100:101], s[34:35]
	s_cbranch_execz .Lpf_skip_g2
	v_readfirstlane_b32 s10, v173
	s_lshl_b32 s10, s10, 7
	s_add_u32 s10, s64, s10
	s_addc_u32 s11, s65, 0
	global_atomic_add v231, v109, v1, s[10:11] sc0

.Lpf_end_g2:
	ds_read_b128 v[2:5], v178
	ds_read_b128 v[6:9], v100
	s_waitcnt vmcnt(12)
	v_cvt_f32_f16_e32 v12, v233
	v_cvt_f32_f16_sdwa v13, v233 dst_sel:DWORD dst_unused:UNUSED_PAD src0_sel:WORD_1
	v_cvt_f32_f16_e32 v10, v232
	v_cvt_f32_f16_sdwa v11, v232 dst_sel:DWORD dst_unused:UNUSED_PAD src0_sel:WORD_1
	s_waitcnt lgkmcnt(1)
	v_pk_fma_f32 v[4:5], v[12:13], v[56:57], v[4:5]
	v_pk_fma_f32 v[2:3], v[10:11], v[54:55], v[2:3]
	v_add_u32_e32 v10, v176, v107
	v_mad_i64_i32 v[10:11], s[2:3], v10, s62, v[110:111]
	v_cvt_f32_f16_e32 v12, v234
	v_cvt_f32_f16_sdwa v13, v234 dst_sel:DWORD dst_unused:UNUSED_PAD src0_sel:WORD_1
	v_cvt_f32_f16_e32 v14, v235
	v_cvt_f32_f16_sdwa v15, v235 dst_sel:DWORD dst_unused:UNUSED_PAD src0_sel:WORD_1
	v_lshl_add_u64 v[10:11], v[10:11], 0, v[116:117]
	global_store_dwordx4 v[10:11], v[2:5], off nt
	s_waitcnt lgkmcnt(0)
	s_nop 0
	v_pk_fma_f32 v[2:3], v[12:13], v[50:51], v[6:7]
	v_add_u32_e32 v6, v99, v107
	v_mad_i64_i32 v[6:7], s[2:3], v6, s62, v[110:111]
	v_pk_fma_f32 v[4:5], v[14:15], v[52:53], v[8:9]
	v_lshl_add_u64 v[10:11], v[6:7], 0, v[114:115]
	ds_read_b128 v[6:9], v162
	v_cvt_f32_f16_e32 v12, v236
	v_cvt_f32_f16_e32 v14, v237
	v_cvt_f32_f16_sdwa v15, v237 dst_sel:DWORD dst_unused:UNUSED_PAD src0_sel:WORD_1
	v_cvt_f32_f16_sdwa v13, v236 dst_sel:DWORD dst_unused:UNUSED_PAD src0_sel:WORD_1
	global_store_dwordx4 v[10:11], v[2:5], off nt
	v_add_u32_e32 v10, v98, v107
	ds_read_b128 v[2:5], v161
	v_mad_i64_i32 v[10:11], s[2:3], v10, s62, v[110:111]
	s_waitcnt lgkmcnt(1)
	v_pk_fma_f32 v[8:9], v[14:15], v[60:61], v[8:9]
	v_pk_fma_f32 v[6:7], v[12:13], v[58:59], v[6:7]
	v_cvt_f32_f16_e32 v12, v238
	v_cvt_f32_f16_e32 v14, v239
	v_cvt_f32_f16_sdwa v15, v239 dst_sel:DWORD dst_unused:UNUSED_PAD src0_sel:WORD_1
	v_cvt_f32_f16_sdwa v13, v238 dst_sel:DWORD dst_unused:UNUSED_PAD src0_sel:WORD_1
	v_lshl_add_u64 v[10:11], v[10:11], 0, v[112:113]
	global_store_dwordx4 v[10:11], v[6:9], off nt
	s_waitcnt lgkmcnt(0)
	v_pk_fma_f32 v[4:5], v[14:15], v[56:57], v[4:5]
	v_pk_fma_f32 v[2:3], v[12:13], v[54:55], v[2:3]
	v_add_u32_e32 v6, v160, v107
	v_mad_i64_i32 v[6:7], s[2:3], v6, s62, v[110:111]
	v_lshl_add_u64 v[10:11], v[6:7], 0, v[70:71]
	ds_read_b128 v[6:9], v159
	v_cvt_f32_f16_e32 v12, v240
	v_cvt_f32_f16_e32 v14, v241
	v_cvt_f32_f16_sdwa v15, v241 dst_sel:DWORD dst_unused:UNUSED_PAD src0_sel:WORD_1
	v_cvt_f32_f16_sdwa v13, v240 dst_sel:DWORD dst_unused:UNUSED_PAD src0_sel:WORD_1
	global_store_dwordx4 v[10:11], v[2:5], off nt
	v_add_u32_e32 v10, v158, v107
	ds_read_b128 v[2:5], v157
	v_mad_i64_i32 v[10:11], s[2:3], v10, s62, v[110:111]
	s_waitcnt lgkmcnt(1)
	v_pk_fma_f32 v[8:9], v[14:15], v[52:53], v[8:9]
	v_pk_fma_f32 v[6:7], v[12:13], v[50:51], v[6:7]
	v_cvt_f32_f16_e32 v12, v242
	v_cvt_f32_f16_e32 v14, v243
	v_cvt_f32_f16_sdwa v15, v243 dst_sel:DWORD dst_unused:UNUSED_PAD src0_sel:WORD_1
	v_cvt_f32_f16_sdwa v13, v242 dst_sel:DWORD dst_unused:UNUSED_PAD src0_sel:WORD_1
	v_lshl_add_u64 v[10:11], v[10:11], 0, v[68:69]
	global_store_dwordx4 v[10:11], v[6:9], off nt
	s_waitcnt lgkmcnt(0)
	v_pk_fma_f32 v[4:5], v[14:15], v[60:61], v[4:5]
	v_pk_fma_f32 v[2:3], v[12:13], v[58:59], v[2:3]
	v_add_u32_e32 v6, v156, v107
	v_mad_i64_i32 v[6:7], s[2:3], v6, s62, v[110:111]
	v_lshl_add_u64 v[10:11], v[6:7], 0, v[72:73]
	ds_read_b128 v[6:9], v155
	v_cvt_f32_f16_e32 v12, v244
	v_cvt_f32_f16_e32 v14, v245
	v_cvt_f32_f16_sdwa v15, v245 dst_sel:DWORD dst_unused:UNUSED_PAD src0_sel:WORD_1
	v_cvt_f32_f16_sdwa v13, v244 dst_sel:DWORD dst_unused:UNUSED_PAD src0_sel:WORD_1
	global_store_dwordx4 v[10:11], v[2:5], off nt
	v_add_u32_e32 v10, v154, v107
	ds_read_b128 v[2:5], v153
	v_mad_i64_i32 v[10:11], s[2:3], v10, s62, v[110:111]
	s_waitcnt lgkmcnt(1)
	v_pk_fma_f32 v[8:9], v[14:15], v[56:57], v[8:9]
	v_pk_fma_f32 v[6:7], v[12:13], v[54:55], v[6:7]
	v_cvt_f32_f16_e32 v12, v246
	v_cvt_f32_f16_e32 v14, v247
	v_cvt_f32_f16_sdwa v15, v247 dst_sel:DWORD dst_unused:UNUSED_PAD src0_sel:WORD_1
	v_cvt_f32_f16_sdwa v13, v246 dst_sel:DWORD dst_unused:UNUSED_PAD src0_sel:WORD_1
	v_lshl_add_u64 v[10:11], v[10:11], 0, v[62:63]
	global_store_dwordx4 v[10:11], v[6:9], off nt
	s_waitcnt lgkmcnt(0)
	v_pk_fma_f32 v[4:5], v[14:15], v[52:53], v[4:5]
	v_pk_fma_f32 v[2:3], v[12:13], v[50:51], v[2:3]
	v_add_u32_e32 v6, v152, v107
	v_mad_i64_i32 v[6:7], s[2:3], v6, s62, v[110:111]
	v_lshl_add_u64 v[10:11], v[6:7], 0, v[66:67]
	ds_read_b128 v[6:9], v151
	v_cvt_f32_f16_e32 v12, v248
	v_cvt_f32_f16_e32 v14, v249
	v_cvt_f32_f16_sdwa v15, v249 dst_sel:DWORD dst_unused:UNUSED_PAD src0_sel:WORD_1
	v_cvt_f32_f16_sdwa v13, v248 dst_sel:DWORD dst_unused:UNUSED_PAD src0_sel:WORD_1
	global_store_dwordx4 v[10:11], v[2:5], off nt
	v_add_u32_e32 v10, v150, v107
	ds_read_b128 v[2:5], v149
	v_mad_i64_i32 v[10:11], s[2:3], v10, s62, v[110:111]
	s_waitcnt lgkmcnt(1)
	v_pk_fma_f32 v[8:9], v[14:15], v[60:61], v[8:9]
	v_pk_fma_f32 v[6:7], v[12:13], v[58:59], v[6:7]
	v_cvt_f32_f16_e32 v12, v250
	v_cvt_f32_f16_e32 v14, v251
	v_cvt_f32_f16_sdwa v15, v251 dst_sel:DWORD dst_unused:UNUSED_PAD src0_sel:WORD_1
	v_cvt_f32_f16_sdwa v13, v250 dst_sel:DWORD dst_unused:UNUSED_PAD src0_sel:WORD_1
	v_lshl_add_u64 v[10:11], v[10:11], 0, v[64:65]
	global_store_dwordx4 v[10:11], v[6:9], off nt
	s_waitcnt lgkmcnt(0)
	v_pk_fma_f32 v[4:5], v[14:15], v[56:57], v[4:5]
	v_pk_fma_f32 v[2:3], v[12:13], v[54:55], v[2:3]
	v_add_u32_e32 v6, v148, v107
	v_mad_i64_i32 v[6:7], s[2:3], v6, s62, v[110:111]
	v_lshl_add_u64 v[10:11], v[6:7], 0, v[76:77]
	ds_read_b128 v[6:9], v147
	v_cvt_f32_f16_e32 v12, v252
	v_cvt_f32_f16_e32 v14, v253
	v_cvt_f32_f16_sdwa v15, v253 dst_sel:DWORD dst_unused:UNUSED_PAD src0_sel:WORD_1
	v_cvt_f32_f16_sdwa v13, v252 dst_sel:DWORD dst_unused:UNUSED_PAD src0_sel:WORD_1
	global_store_dwordx4 v[10:11], v[2:5], off nt
	ds_read_b128 v[2:5], v137
	v_add_u32_e32 v10, v146, v107
	s_waitcnt lgkmcnt(1)
	v_pk_fma_f32 v[8:9], v[14:15], v[52:53], v[8:9]
	v_pk_fma_f32 v[6:7], v[12:13], v[50:51], v[6:7]
	v_mad_i64_i32 v[10:11], s[2:3], v10, s62, v[110:111]
	v_cvt_f32_f16_e32 v12, v254
	v_cvt_f32_f16_e32 v14, v255
	v_cvt_f32_f16_sdwa v15, v255 dst_sel:DWORD dst_unused:UNUSED_PAD src0_sel:WORD_1
	v_cvt_f32_f16_sdwa v13, v254 dst_sel:DWORD dst_unused:UNUSED_PAD src0_sel:WORD_1
	v_lshl_add_u64 v[10:11], v[10:11], 0, v[74:75]
	global_store_dwordx4 v[10:11], v[6:9], off nt
	s_waitcnt lgkmcnt(0)
	v_pk_fma_f32 v[4:5], v[14:15], v[60:61], v[4:5]
	v_pk_fma_f32 v[2:3], v[12:13], v[58:59], v[2:3]
	v_add_u32_e32 v6, v136, v107
	v_mad_i64_i32 v[6:7], s[2:3], v6, s62, v[110:111]
	v_lshl_add_u64 v[6:7], v[6:7], 0, v[78:79]
	global_store_dwordx4 v[6:7], v[2:5], off nt

.LBB1_66:
	ds_read_b128 v[148:151], v144
	ds_read_b128 v[152:155], v144 offset:1024
	ds_read_b128 v[156:159], v144 offset:2048
	ds_read_b128 v[160:163], v144 offset:3072
	ds_read_b128 v[164:167], v144 offset:4096
	ds_read_b128 v[174:177], v144 offset:5120
	v_add_u32_e32 v145, 0xc000, v129
	v_lshl_add_u64 v[218:219], v[112:113], 0, s[0:1]
	v_readfirstlane_b32 s3, v145
	v_lshl_add_u64 v[146:147], v[218:219], 0, s[78:79]
	s_mov_b32 m0, s3
	ds_read_b128 v[178:181], v130
	ds_read_b128 v[182:185], v130 offset:1024
	ds_read_b128 v[186:189], v108
	ds_read_b128 v[190:193], v108 offset:1024
	global_load_lds_dwordx4 v[146:147], off
	v_add_u32_e32 v146, 0xe000, v129
	v_lshl_add_u64 v[220:221], v[114:115], 0, s[0:1]
	v_readfirstlane_b32 s3, v146
	v_lshl_add_u64 v[194:195], v[220:221], 0, s[78:79]
	s_mov_b32 m0, s3
	s_nop 0
	global_load_lds_dwordx4 v[194:195], off
	s_waitcnt lgkmcnt(4)
	s_barrier
	s_waitcnt lgkmcnt(0)
	s_setprio 1
	s_waitcnt lgkmcnt(0)
	v_mfma_f32_16x16x32_f16 v[94:97], v[178:181], v[148:151], v[94:97]
	v_mfma_f32_16x16x32_f16 v[90:93], v[178:181], v[156:159], v[90:93]
	v_mfma_f32_16x16x32_f16 v[86:89], v[178:181], v[164:167], v[86:89]
	v_mfma_f32_16x16x32_f16 v[74:77], v[186:189], v[148:151], v[74:77]
	v_mfma_f32_16x16x32_f16 v[46:49], v[186:189], v[156:159], v[46:49]
	v_mfma_f32_16x16x32_f16 v[18:21], v[186:189], v[164:167], v[18:21]
	v_mfma_f32_16x16x32_f16 v[94:97], v[182:185], v[152:155], v[94:97]
	v_mfma_f32_16x16x32_f16 v[90:93], v[182:185], v[160:163], v[90:93]
	v_mfma_f32_16x16x32_f16 v[86:89], v[182:185], v[174:177], v[86:89]
	v_mfma_f32_16x16x32_f16 v[74:77], v[190:193], v[152:155], v[74:77]
	v_mfma_f32_16x16x32_f16 v[46:49], v[190:193], v[160:163], v[46:49]
	v_mfma_f32_16x16x32_f16 v[18:21], v[190:193], v[174:177], v[18:21]
	s_setprio 0
	s_barrier
	v_lshl_add_u64 v[222:223], v[104:105], 0, s[0:1]
	v_readfirstlane_b32 s3, v128
	v_lshl_add_u64 v[224:225], v[222:223], 0, s[80:81]
	s_mov_b32 m0, s3
	v_add_u32_e32 v147, 0x2000, v128
	ds_read_b128 v[194:197], v143
	ds_read_b128 v[198:201], v143 offset:1024
	ds_read_b128 v[202:205], v143 offset:2048
	ds_read_b128 v[206:209], v143 offset:3072
	ds_read_b128 v[210:213], v143 offset:4096
	ds_read_b128 v[214:217], v143 offset:5120
	global_load_lds_dwordx4 v[224:225], off
	v_lshl_add_u64 v[224:225], v[110:111], 0, s[0:1]
	v_readfirstlane_b32 s3, v147
	v_lshl_add_u64 v[226:227], v[224:225], 0, s[80:81]
	s_mov_b32 m0, s3
	s_nop 0
	global_load_lds_dwordx4 v[226:227], off
	s_barrier
	s_waitcnt lgkmcnt(0)
	s_setprio 1
	s_waitcnt lgkmcnt(0)
	v_mfma_f32_16x16x32_f16 v[10:13], v[178:181], v[194:197], v[10:13]
	v_mfma_f32_16x16x32_f16 v[6:9], v[178:181], v[202:205], v[6:9]
	v_mfma_f32_16x16x32_f16 v[2:5], v[178:181], v[210:213], v[2:5]
	v_mfma_f32_16x16x32_f16 v[26:29], v[186:189], v[194:197], v[26:29]
	v_mfma_f32_16x16x32_f16 v[34:37], v[186:189], v[202:205], v[34:37]
	v_mfma_f32_16x16x32_f16 v[50:53], v[186:189], v[210:213], v[50:53]
	v_mfma_f32_16x16x32_f16 v[10:13], v[182:185], v[198:201], v[10:13]
	v_mfma_f32_16x16x32_f16 v[6:9], v[182:185], v[206:209], v[6:9]
	v_mfma_f32_16x16x32_f16 v[2:5], v[182:185], v[214:217], v[2:5]
	v_mfma_f32_16x16x32_f16 v[26:29], v[190:193], v[198:201], v[26:29]
	v_mfma_f32_16x16x32_f16 v[34:37], v[190:193], v[206:209], v[34:37]
	v_mfma_f32_16x16x32_f16 v[50:53], v[190:193], v[214:217], v[50:53]
	s_setprio 0
	v_readfirstlane_b32 s3, v129
	v_lshl_add_u64 v[226:227], v[218:219], 0, s[80:81]
	s_mov_b32 m0, s3
	v_readfirstlane_b32 s3, v131
	s_barrier
	ds_read_b128 v[178:181], v130 offset:16384
	ds_read_b128 v[182:185], v130 offset:17408
	ds_read_b128 v[186:189], v108 offset:16384
	ds_read_b128 v[190:193], v108 offset:17408
	global_load_lds_dwordx4 v[226:227], off
	v_lshl_add_u64 v[226:227], v[220:221], 0, s[80:81]
	s_mov_b32 m0, s3
	s_nop 0
	global_load_lds_dwordx4 v[226:227], off
	s_barrier
	s_waitcnt lgkmcnt(0)
	s_setprio 1
	s_waitcnt lgkmcnt(0)
	v_mfma_f32_16x16x32_f16 v[14:17], v[178:181], v[148:151], v[14:17]
	v_mfma_f32_16x16x32_f16 v[22:25], v[178:181], v[156:159], v[22:25]
	v_mfma_f32_16x16x32_f16 v[30:33], v[178:181], v[164:167], v[30:33]
	v_mfma_f32_16x16x32_f16 v[38:41], v[186:189], v[148:151], v[38:41]
	v_mfma_f32_16x16x32_f16 v[54:57], v[186:189], v[156:159], v[54:57]
	v_mfma_f32_16x16x32_f16 v[62:65], v[186:189], v[164:167], v[62:65]
	v_mfma_f32_16x16x32_f16 v[14:17], v[182:185], v[152:155], v[14:17]
	v_mfma_f32_16x16x32_f16 v[22:25], v[182:185], v[160:163], v[22:25]
	v_mfma_f32_16x16x32_f16 v[30:33], v[182:185], v[174:177], v[30:33]
	v_mfma_f32_16x16x32_f16 v[38:41], v[190:193], v[152:155], v[38:41]
	v_mfma_f32_16x16x32_f16 v[54:57], v[190:193], v[160:163], v[54:57]
	v_mfma_f32_16x16x32_f16 v[62:65], v[190:193], v[174:177], v[62:65]
	s_setprio 0
	s_barrier
	v_lshl_add_u64 v[226:227], v[116:117], 0, s[0:1]
	v_readfirstlane_b32 s3, v132
	v_add_u32_e32 v147, 0x2000, v132
	v_lshl_add_u64 v[148:149], v[226:227], 0, s[82:83]
	s_mov_b32 m0, s3
	v_lshl_add_u64 v[228:229], v[118:119], 0, s[0:1]
	v_readfirstlane_b32 s3, v147
	global_load_lds_dwordx4 v[148:149], off
	v_lshl_add_u64 v[148:149], v[228:229], 0, s[82:83]
	s_mov_b32 m0, s3
	s_nop 0
	global_load_lds_dwordx4 v[148:149], off
	s_waitcnt vmcnt(6)
	s_barrier
	s_setprio 1
	v_mfma_f32_16x16x32_f16 v[42:45], v[178:181], v[194:197], v[42:45]
	v_mfma_f32_16x16x32_f16 v[58:61], v[178:181], v[202:205], v[58:61]
	v_mfma_f32_16x16x32_f16 v[66:69], v[178:181], v[210:213], v[66:69]
	v_mfma_f32_16x16x32_f16 v[70:73], v[186:189], v[194:197], v[70:73]
	v_mfma_f32_16x16x32_f16 v[78:81], v[186:189], v[202:205], v[78:81]
	v_mfma_f32_16x16x32_f16 v[82:85], v[186:189], v[210:213], v[82:85]
	v_mfma_f32_16x16x32_f16 v[42:45], v[182:185], v[198:201], v[42:45]
	v_mfma_f32_16x16x32_f16 v[58:61], v[182:185], v[206:209], v[58:61]
	v_mfma_f32_16x16x32_f16 v[66:69], v[182:185], v[214:217], v[66:69]
	v_mfma_f32_16x16x32_f16 v[70:73], v[190:193], v[198:201], v[70:73]
	v_mfma_f32_16x16x32_f16 v[78:81], v[190:193], v[206:209], v[78:81]
	v_mfma_f32_16x16x32_f16 v[82:85], v[190:193], v[214:217], v[82:85]
	s_setprio 0
	s_barrier
	ds_read_b128 v[148:151], v136
	ds_read_b128 v[152:155], v136 offset:1024
	ds_read_b128 v[156:159], v136 offset:2048
	ds_read_b128 v[160:163], v136 offset:3072
	ds_read_b128 v[164:167], v136 offset:4096
	ds_read_b128 v[174:177], v136 offset:5120
	v_readfirstlane_b32 s3, v134
	v_lshl_add_u64 v[194:195], v[218:219], 0, s[84:85]
	s_mov_b32 m0, s3
	v_readfirstlane_b32 s3, v135
	ds_read_b128 v[178:181], v130 offset:32768
	ds_read_b128 v[182:185], v130 offset:33792
	ds_read_b128 v[186:189], v108 offset:32768
	ds_read_b128 v[190:193], v108 offset:33792
	global_load_lds_dwordx4 v[194:195], off
	v_lshl_add_u64 v[194:195], v[220:221], 0, s[84:85]
	s_mov_b32 m0, s3
	s_nop 0
	global_load_lds_dwordx4 v[194:195], off
	s_waitcnt lgkmcnt(4)
	s_barrier
	s_waitcnt lgkmcnt(0)
	s_setprio 1
	s_waitcnt lgkmcnt(0)
	v_mfma_f32_16x16x32_f16 v[94:97], v[178:181], v[148:151], v[94:97]
	v_mfma_f32_16x16x32_f16 v[90:93], v[178:181], v[156:159], v[90:93]
	v_mfma_f32_16x16x32_f16 v[86:89], v[178:181], v[164:167], v[86:89]
	v_mfma_f32_16x16x32_f16 v[74:77], v[186:189], v[148:151], v[74:77]
	v_mfma_f32_16x16x32_f16 v[46:49], v[186:189], v[156:159], v[46:49]
	v_mfma_f32_16x16x32_f16 v[18:21], v[186:189], v[164:167], v[18:21]
	v_mfma_f32_16x16x32_f16 v[94:97], v[182:185], v[152:155], v[94:97]
	v_mfma_f32_16x16x32_f16 v[90:93], v[182:185], v[160:163], v[90:93]
	v_mfma_f32_16x16x32_f16 v[86:89], v[182:185], v[174:177], v[86:89]
	v_mfma_f32_16x16x32_f16 v[74:77], v[190:193], v[152:155], v[74:77]
	v_mfma_f32_16x16x32_f16 v[46:49], v[190:193], v[160:163], v[46:49]
	v_mfma_f32_16x16x32_f16 v[18:21], v[190:193], v[174:177], v[18:21]
	s_setprio 0
	s_barrier
	v_readfirstlane_b32 s3, v137
	v_lshl_add_u64 v[222:223], v[222:223], 0, s[86:87]
	s_mov_b32 m0, s3
	v_readfirstlane_b32 s3, v138
	ds_read_b128 v[194:197], v133
	ds_read_b128 v[198:201], v133 offset:1024
	ds_read_b128 v[202:205], v133 offset:2048
	ds_read_b128 v[206:209], v133 offset:3072
	ds_read_b128 v[210:213], v133 offset:4096
	ds_read_b128 v[214:217], v133 offset:5120
	global_load_lds_dwordx4 v[222:223], off
	v_lshl_add_u64 v[222:223], v[224:225], 0, s[86:87]
	s_mov_b32 m0, s3
	s_nop 0
	global_load_lds_dwordx4 v[222:223], off
	s_barrier
	s_waitcnt lgkmcnt(0)
	s_setprio 1
	s_waitcnt lgkmcnt(0)
	v_mfma_f32_16x16x32_f16 v[10:13], v[178:181], v[194:197], v[10:13]
	v_mfma_f32_16x16x32_f16 v[6:9], v[178:181], v[202:205], v[6:9]
	v_mfma_f32_16x16x32_f16 v[2:5], v[178:181], v[210:213], v[2:5]
	v_mfma_f32_16x16x32_f16 v[26:29], v[186:189], v[194:197], v[26:29]
	v_mfma_f32_16x16x32_f16 v[34:37], v[186:189], v[202:205], v[34:37]
	v_mfma_f32_16x16x32_f16 v[50:53], v[186:189], v[210:213], v[50:53]
	v_mfma_f32_16x16x32_f16 v[10:13], v[182:185], v[198:201], v[10:13]
	v_mfma_f32_16x16x32_f16 v[6:9], v[182:185], v[206:209], v[6:9]
	v_mfma_f32_16x16x32_f16 v[2:5], v[182:185], v[214:217], v[2:5]
	v_mfma_f32_16x16x32_f16 v[26:29], v[190:193], v[198:201], v[26:29]
	v_mfma_f32_16x16x32_f16 v[34:37], v[190:193], v[206:209], v[34:37]
	v_mfma_f32_16x16x32_f16 v[50:53], v[190:193], v[214:217], v[50:53]
	s_setprio 0
	v_readfirstlane_b32 s3, v139
	v_lshl_add_u64 v[218:219], v[218:219], 0, s[86:87]
	s_mov_b32 m0, s3
	v_readfirstlane_b32 s3, v140
	s_barrier
	ds_read_b128 v[178:181], v130 offset:49152
	ds_read_b128 v[182:185], v130 offset:50176
	ds_read_b128 v[186:189], v108 offset:49152
	ds_read_b128 v[190:193], v108 offset:50176
	global_load_lds_dwordx4 v[218:219], off
	v_lshl_add_u64 v[218:219], v[220:221], 0, s[86:87]
	s_mov_b32 m0, s3
	s_nop 0
	global_load_lds_dwordx4 v[218:219], off
	s_barrier
	s_waitcnt lgkmcnt(0)
	s_setprio 1
	s_waitcnt lgkmcnt(0)
	v_mfma_f32_16x16x32_f16 v[14:17], v[178:181], v[148:151], v[14:17]
	v_mfma_f32_16x16x32_f16 v[22:25], v[178:181], v[156:159], v[22:25]
	v_mfma_f32_16x16x32_f16 v[30:33], v[178:181], v[164:167], v[30:33]
	v_mfma_f32_16x16x32_f16 v[38:41], v[186:189], v[148:151], v[38:41]
	v_mfma_f32_16x16x32_f16 v[54:57], v[186:189], v[156:159], v[54:57]
	v_mfma_f32_16x16x32_f16 v[62:65], v[186:189], v[164:167], v[62:65]
	v_mfma_f32_16x16x32_f16 v[14:17], v[182:185], v[152:155], v[14:17]
	v_mfma_f32_16x16x32_f16 v[22:25], v[182:185], v[160:163], v[22:25]
	v_mfma_f32_16x16x32_f16 v[30:33], v[182:185], v[174:177], v[30:33]
	v_mfma_f32_16x16x32_f16 v[38:41], v[190:193], v[152:155], v[38:41]
	v_mfma_f32_16x16x32_f16 v[54:57], v[190:193], v[160:163], v[54:57]
	v_mfma_f32_16x16x32_f16 v[62:65], v[190:193], v[174:177], v[62:65]
	s_setprio 0
	s_barrier
	v_readfirstlane_b32 s3, v141
	v_lshl_add_u64 v[148:149], v[226:227], 0, s[88:89]
	s_mov_b32 m0, s3
	v_readfirstlane_b32 s3, v142
	global_load_lds_dwordx4 v[148:149], off
	v_lshl_add_u64 v[148:149], v[228:229], 0, s[88:89]
	s_mov_b32 m0, s3
	s_nop 0
	global_load_lds_dwordx4 v[148:149], off
	s_waitcnt vmcnt(6)
	s_barrier
	s_setprio 1
	v_mfma_f32_16x16x32_f16 v[42:45], v[178:181], v[194:197], v[42:45]
	v_mfma_f32_16x16x32_f16 v[58:61], v[178:181], v[202:205], v[58:61]
	v_mfma_f32_16x16x32_f16 v[66:69], v[178:181], v[210:213], v[66:69]
	v_mfma_f32_16x16x32_f16 v[70:73], v[186:189], v[194:197], v[70:73]
	v_mfma_f32_16x16x32_f16 v[78:81], v[186:189], v[202:205], v[78:81]
	v_mfma_f32_16x16x32_f16 v[82:85], v[186:189], v[210:213], v[82:85]
	v_mfma_f32_16x16x32_f16 v[42:45], v[182:185], v[198:201], v[42:45]
	v_mfma_f32_16x16x32_f16 v[58:61], v[182:185], v[206:209], v[58:61]
	v_mfma_f32_16x16x32_f16 v[66:69], v[182:185], v[214:217], v[66:69]
	v_mfma_f32_16x16x32_f16 v[70:73], v[190:193], v[198:201], v[70:73]
	v_mfma_f32_16x16x32_f16 v[78:81], v[190:193], v[206:209], v[78:81]
	v_mfma_f32_16x16x32_f16 v[82:85], v[190:193], v[214:217], v[82:85]
	s_setprio 0
	s_add_i32 s2, s2, 2
	s_add_u32 s0, s0, 0x100
	s_addc_u32 s1, s1, 0
	s_cmp_lt_u32 s2, 8
	s_barrier
	s_cbranch_scc1 .LBB1_66
	v_readlane_b32 s10, v230, 2
	v_readlane_b32 s11, v230, 3
	v_or_b32_e32 v238, v126, v125
	v_add_u32_e32 v238, v238, v121
	v_lshlrev_b32_e32 v232, 1, v238
	v_and_b32_e32 v232, -4, v232
	v_add_u32_e32 v233, 16, v238
	v_lshlrev_b32_e32 v233, 1, v233
	v_and_b32_e32 v233, -4, v233
	v_add_u32_e32 v234, 32, v238
	v_lshlrev_b32_e32 v234, 1, v234
	v_and_b32_e32 v234, -4, v234
	v_add_u32_e32 v235, 0x60, v238
	v_lshlrev_b32_e32 v235, 1, v235
	v_and_b32_e32 v235, -4, v235
	v_add_u32_e32 v236, 0x70, v238
	v_lshlrev_b32_e32 v236, 1, v236
	v_and_b32_e32 v236, -4, v236
	v_add_u32_e32 v237, 0x80, v238
	v_lshlrev_b32_e32 v237, 1, v237
	v_and_b32_e32 v237, -4, v237
	global_load_dword v232, v232, s[48:49]
	global_load_dword v233, v233, s[48:49]
	global_load_dword v234, v234, s[48:49]
	global_load_dword v235, v235, s[48:49]
	global_load_dword v236, v236, s[48:49]
	global_load_dword v237, v237, s[48:49]
	s_mov_b32 s32, 0x2aaaaaab
	v_mul_hi_u32 v239, v107, s32
	v_lshrrev_b32_e32 v239, 4, v239
	v_mul_u32_u24_e32 v239, 0x60, v239
	v_sub_u32_e32 v239, v107, v239
	v_lshrrev_b32_e32 v240, 1, v121
	v_add_u32_e32 v239, v239, v240
	v_lshlrev_b32_e32 v239, 3, v239
	global_load_dwordx2 v[240:241], v239, s[10:11]
	global_load_dwordx2 v[242:243], v239, s[10:11] offset:3072
	s_mov_b64 s[2:3], 0x580
	v_readfirstlane_b32 s0, v145
	v_lshl_add_u64 v[100:101], v[100:101], 0, s[2:3]
	s_mov_b32 m0, s0
	v_readfirstlane_b32 s0, v146
	ds_read_b128 v[110:113], v144
	ds_read_b128 v[114:117], v144 offset:1024
	ds_read_b128 v[138:141], v144 offset:2048
	ds_read_b128 v[148:151], v144 offset:3072
	ds_read_b128 v[152:155], v144 offset:4096
	ds_read_b128 v[156:159], v144 offset:5120
	ds_read_b128 v[160:163], v130
	ds_read_b128 v[164:167], v130 offset:1024
	ds_read_b128 v[174:177], v108
	ds_read_b128 v[178:181], v108 offset:1024
	global_load_lds_dwordx4 v[100:101], off
	v_lshl_add_u64 v[100:101], v[102:103], 0, s[2:3]
	s_mov_b32 m0, s0
	s_nop 0
	global_load_lds_dwordx4 v[100:101], off
	s_barrier
	s_waitcnt lgkmcnt(0)
	s_setprio 1
	s_waitcnt lgkmcnt(0)
	v_mfma_f32_16x16x32_f16 v[94:97], v[160:163], v[110:113], v[94:97]
	v_mfma_f32_16x16x32_f16 v[90:93], v[160:163], v[138:141], v[90:93]
	v_mfma_f32_16x16x32_f16 v[86:89], v[160:163], v[152:155], v[86:89]
	v_mfma_f32_16x16x32_f16 v[74:77], v[174:177], v[110:113], v[74:77]
	v_mfma_f32_16x16x32_f16 v[18:21], v[174:177], v[152:155], v[18:21]
	v_mfma_f32_16x16x32_f16 v[94:97], v[164:167], v[114:117], v[94:97]
	v_mfma_f32_16x16x32_f16 v[90:93], v[164:167], v[148:151], v[90:93]
	v_mfma_f32_16x16x32_f16 v[86:89], v[164:167], v[156:159], v[86:89]
	v_mfma_f32_16x16x32_f16 v[74:77], v[178:181], v[114:117], v[74:77]
	v_mfma_f32_16x16x32_f16 v[46:49], v[174:177], v[138:141], v[46:49]
	v_mfma_f32_16x16x32_f16 v[18:21], v[178:181], v[156:159], v[18:21]
	v_mfma_f32_16x16x32_f16 v[100:103], v[178:181], v[148:151], v[46:49]
	s_setprio 0
	s_barrier
	s_nop 3
	ds_read_b128 v[46:49], v143
	ds_read_b128 v[144:147], v143 offset:1024
	ds_read_b128 v[182:185], v143 offset:2048
	ds_read_b128 v[186:189], v143 offset:3072
	ds_read_b128 v[190:193], v143 offset:4096
	ds_read_b128 v[194:197], v143 offset:5120
	s_barrier
	s_waitcnt lgkmcnt(0)
	s_setprio 1
	s_waitcnt lgkmcnt(0)
	v_mfma_f32_16x16x32_f16 v[34:37], v[174:177], v[182:185], v[34:37]
	v_mfma_f32_16x16x32_f16 v[10:13], v[160:163], v[46:49], v[10:13]
	v_mfma_f32_16x16x32_f16 v[6:9], v[160:163], v[182:185], v[6:9]
	v_mfma_f32_16x16x32_f16 v[2:5], v[160:163], v[190:193], v[2:5]
	v_mfma_f32_16x16x32_f16 v[26:29], v[174:177], v[46:49], v[26:29]
	v_mfma_f32_16x16x32_f16 v[160:163], v[178:181], v[186:189], v[34:37]
	v_mfma_f32_16x16x32_f16 v[34:37], v[174:177], v[190:193], v[50:53]
	v_mfma_f32_16x16x32_f16 v[10:13], v[164:167], v[144:147], v[10:13]
	v_mfma_f32_16x16x32_f16 v[6:9], v[164:167], v[186:189], v[6:9]
	v_mfma_f32_16x16x32_f16 v[2:5], v[164:167], v[194:197], v[2:5]
	v_mfma_f32_16x16x32_f16 v[26:29], v[178:181], v[144:147], v[26:29]
	v_mfma_f32_16x16x32_f16 v[50:53], v[178:181], v[194:197], v[34:37]
	s_setprio 0
	s_barrier
	s_nop 0
	ds_read_b128 v[34:37], v130 offset:16384
	ds_read_b128 v[164:167], v130 offset:17408
	ds_read_b128 v[174:177], v108 offset:16384
	ds_read_b128 v[178:181], v108 offset:17408
	s_waitcnt vmcnt(12)
	s_barrier
	s_waitcnt lgkmcnt(0)
	s_setprio 1
	s_waitcnt lgkmcnt(0)
	v_mfma_f32_16x16x32_f16 v[22:25], v[34:37], v[138:141], v[22:25]
	v_mfma_f32_16x16x32_f16 v[198:201], v[164:167], v[148:151], v[22:25]
	v_mfma_f32_16x16x32_f16 v[22:25], v[34:37], v[152:155], v[30:33]
	v_mfma_f32_16x16x32_f16 v[30:33], v[164:167], v[156:159], v[22:25]
	v_mfma_f32_16x16x32_f16 v[22:25], v[174:177], v[110:113], v[38:41]
	v_mfma_f32_16x16x32_f16 v[14:17], v[34:37], v[110:113], v[14:17]
	v_mfma_f32_16x16x32_f16 v[110:113], v[178:181], v[114:117], v[22:25]
	v_mfma_f32_16x16x32_f16 v[22:25], v[174:177], v[138:141], v[54:57]
	v_mfma_f32_16x16x32_f16 v[14:17], v[164:167], v[114:117], v[14:17]
	v_mfma_f32_16x16x32_f16 v[54:57], v[178:181], v[148:151], v[22:25]
	v_mfma_f32_16x16x32_f16 v[22:25], v[174:177], v[152:155], v[62:65]
	v_mfma_f32_16x16x32_f16 v[114:117], v[178:181], v[156:159], v[22:25]
	s_setprio 0
	s_setprio 1
	v_mfma_f32_16x16x32_f16 v[22:25], v[34:37], v[46:49], v[42:45]
	v_mfma_f32_16x16x32_f16 v[138:141], v[164:167], v[144:147], v[22:25]
	v_mfma_f32_16x16x32_f16 v[22:25], v[34:37], v[182:185], v[58:61]
	v_mfma_f32_16x16x32_f16 v[148:151], v[164:167], v[186:189], v[22:25]
	v_mfma_f32_16x16x32_f16 v[22:25], v[34:37], v[190:193], v[66:69]
	v_mfma_f32_16x16x32_f16 v[152:155], v[164:167], v[194:197], v[22:25]
	v_mfma_f32_16x16x32_f16 v[22:25], v[174:177], v[46:49], v[70:73]
	v_mfma_f32_16x16x32_f16 v[142:145], v[178:181], v[144:147], v[22:25]
	v_mfma_f32_16x16x32_f16 v[22:25], v[174:177], v[182:185], v[78:81]
	v_mfma_f32_16x16x32_f16 v[156:159], v[178:181], v[186:189], v[22:25]
	v_mfma_f32_16x16x32_f16 v[22:25], v[174:177], v[190:193], v[82:85]
	v_mfma_f32_16x16x32_f16 v[164:167], v[178:181], v[194:197], v[22:25]
	s_setprio 0
	s_barrier
	ds_read_b128 v[58:61], v136
	ds_read_b128 v[174:177], v136 offset:1024
	ds_read_b128 v[178:181], v136 offset:2048
	ds_read_b128 v[182:185], v136 offset:3072
	ds_read_b128 v[186:189], v136 offset:4096
	ds_read_b128 v[134:137], v136 offset:5120
	ds_read_b128 v[34:37], v130 offset:32768
	ds_read_b128 v[62:65], v130 offset:33792
	ds_read_b128 v[78:81], v108 offset:32768
	ds_read_b128 v[190:193], v108 offset:33792
	s_waitcnt vmcnt(2)
	s_barrier
	s_waitcnt lgkmcnt(0)
	s_setprio 1
	s_waitcnt lgkmcnt(0)
	v_mfma_f32_16x16x32_f16 v[22:25], v[34:37], v[58:61], v[94:97]
	v_mfma_f32_16x16x32_f16 v[82:85], v[62:65], v[174:177], v[22:25]
	v_mfma_f32_16x16x32_f16 v[22:25], v[34:37], v[178:181], v[90:93]
	v_mfma_f32_16x16x32_f16 v[70:73], v[62:65], v[182:185], v[22:25]
	v_mfma_f32_16x16x32_f16 v[22:25], v[34:37], v[186:189], v[86:89]
	v_mfma_f32_16x16x32_f16 v[46:49], v[62:65], v[134:137], v[22:25]
	v_mfma_f32_16x16x32_f16 v[22:25], v[78:81], v[58:61], v[74:77]
	v_mfma_f32_16x16x32_f16 v[86:89], v[190:193], v[174:177], v[22:25]
	v_mfma_f32_16x16x32_f16 v[22:25], v[78:81], v[178:181], v[100:103]
	v_mfma_f32_16x16x32_f16 v[18:21], v[78:81], v[186:189], v[18:21]
	v_mfma_f32_16x16x32_f16 v[66:69], v[190:193], v[182:185], v[22:25]
	v_mfma_f32_16x16x32_f16 v[42:45], v[190:193], v[134:137], v[18:21]
	s_setprio 0
	s_barrier
	ds_read_b128 v[100:103], v133
	ds_read_b128 v[194:197], v133 offset:1024
	ds_read_b128 v[202:205], v133 offset:2048
	ds_read_b128 v[206:209], v133 offset:3072
	ds_read_b128 v[210:213], v133 offset:4096
	ds_read_b128 v[214:217], v133 offset:5120
	s_waitcnt vmcnt(0)
	s_barrier
	s_waitcnt lgkmcnt(0)
	s_setprio 1
	s_waitcnt lgkmcnt(0)
	v_mfma_f32_16x16x32_f16 v[6:9], v[34:37], v[202:205], v[6:9]
	v_mfma_f32_16x16x32_f16 v[2:5], v[34:37], v[210:213], v[2:5]
	v_mfma_f32_16x16x32_f16 v[22:25], v[62:65], v[206:209], v[6:9]
	v_mfma_f32_16x16x32_f16 v[6:9], v[62:65], v[214:217], v[2:5]
	v_mfma_f32_16x16x32_f16 v[2:5], v[78:81], v[100:103], v[26:29]
	v_mfma_f32_16x16x32_f16 v[10:13], v[34:37], v[100:103], v[10:13]
	v_mfma_f32_16x16x32_f16 v[34:37], v[190:193], v[194:197], v[2:5]
	v_mfma_f32_16x16x32_f16 v[2:5], v[78:81], v[202:205], v[160:163]
	v_mfma_f32_16x16x32_f16 v[18:21], v[190:193], v[206:209], v[2:5]
	v_mfma_f32_16x16x32_f16 v[2:5], v[78:81], v[210:213], v[50:53]
	v_mfma_f32_16x16x32_f16 v[38:41], v[62:65], v[194:197], v[10:13]
	v_mfma_f32_16x16x32_f16 v[2:5], v[190:193], v[214:217], v[2:5]
	s_setprio 0
	s_barrier
	ds_read_b128 v[10:13], v130 offset:49152
	ds_read_b128 v[26:29], v130 offset:50176
	ds_read_b128 v[128:131], v108 offset:49152
	ds_read_b128 v[160:163], v108 offset:50176
	s_barrier
	s_waitcnt lgkmcnt(0)
	s_setprio 1
	s_waitcnt lgkmcnt(0)
	v_mfma_f32_16x16x32_f16 v[14:17], v[10:13], v[58:61], v[14:17]
	v_mfma_f32_16x16x32_f16 v[90:93], v[26:29], v[174:177], v[14:17]
	v_mfma_f32_16x16x32_f16 v[14:17], v[10:13], v[178:181], v[198:201]
	v_mfma_f32_16x16x32_f16 v[78:81], v[26:29], v[182:185], v[14:17]
	v_mfma_f32_16x16x32_f16 v[14:17], v[10:13], v[186:189], v[30:33]
	v_mfma_f32_16x16x32_f16 v[62:65], v[26:29], v[134:137], v[14:17]
	v_mfma_f32_16x16x32_f16 v[14:17], v[128:131], v[58:61], v[110:113]
	v_mfma_f32_16x16x32_f16 v[94:97], v[160:163], v[174:177], v[14:17]
	v_mfma_f32_16x16x32_f16 v[14:17], v[128:131], v[178:181], v[54:57]
	v_mfma_f32_16x16x32_f16 v[74:77], v[160:163], v[182:185], v[14:17]
	v_mfma_f32_16x16x32_f16 v[14:17], v[128:131], v[186:189], v[114:117]
	v_mfma_f32_16x16x32_f16 v[58:61], v[160:163], v[134:137], v[14:17]
	s_setprio 0
	s_setprio 1
	v_mfma_f32_16x16x32_f16 v[14:17], v[10:13], v[100:103], v[138:141]
	v_mfma_f32_16x16x32_f16 v[54:57], v[26:29], v[194:197], v[14:17]
	v_mfma_f32_16x16x32_f16 v[14:17], v[10:13], v[202:205], v[148:151]
	v_mfma_f32_16x16x32_f16 v[10:13], v[10:13], v[210:213], v[152:155]
	v_mfma_f32_16x16x32_f16 v[30:33], v[26:29], v[206:209], v[14:17]
	v_mfma_f32_16x16x32_f16 v[14:17], v[26:29], v[214:217], v[10:13]
	v_mfma_f32_16x16x32_f16 v[10:13], v[128:131], v[100:103], v[142:145]
	v_mfma_f32_16x16x32_f16 v[50:53], v[160:163], v[194:197], v[10:13]
	v_mfma_f32_16x16x32_f16 v[10:13], v[128:131], v[202:205], v[156:159]
	v_mfma_f32_16x16x32_f16 v[26:29], v[160:163], v[206:209], v[10:13]
	v_mfma_f32_16x16x32_f16 v[10:13], v[128:131], v[210:213], v[164:167]
	v_mfma_f32_16x16x32_f16 v[10:13], v[160:163], v[214:217], v[10:13]
	s_setprio 0
	s_movk_i32 s0, 0x100
	v_cmp_gt_u32_e64 s[0:1], s0, v107
	s_barrier
	s_and_saveexec_b64 s[2:3], s[0:1]
	s_cbranch_execz .LBB1_69
	s_barrier
.LBB1_69:
	s_or_b64 exec, exec, s[2:3]
	v_or_b32_e32 v100, v126, v125
	v_add_u32_e32 v104, 16, v100
	v_or_b32_e32 v101, v100, v121
	v_add_u16_e32 v102, v104, v121
	v_lshlrev_b32_e32 v101, 1, v101
	v_lshrrev_b16_e32 v102, 1, v102
	v_and_b32_e32 v101, 0x7fc, v101
	v_lshlrev_b32_e32 v102, 2, v102
	s_waitcnt vmcnt(0)
	s_barrier
	v_mov_b32_e32 v101, v232
	v_lshrrev_b32_e32 v103, 2, v107
	v_mov_b32_e32 v102, v233
	v_bitop3_b32 v108, v126, v124, v125 bitop3:0x36
	v_and_or_b32 v105, v103, 12, v127
	v_lshlrev_b32_e32 v103, 1, v108
	v_add_u32_e32 v108, 32, v100
	v_add_u16_e32 v113, v108, v121
	v_lshrrev_b16_e32 v113, 1, v113
	v_lshlrev_b32_e32 v113, 2, v113
	v_mov_b32_e32 v113, v234
	v_add_u32_e32 v110, 0x60, v100
	v_add_u32_e32 v111, 0x70, v100
	s_movk_i32 s1, 0x180
	v_or_b32_e32 v112, 0x80, v100
	v_mul_lo_u32 v105, v105, s1
	v_xor_b32_e32 v104, v104, v124
	v_add_u16_e32 v114, v110, v121
	v_add_u16_e32 v115, v111, v121
	v_add_u16_e32 v112, v112, v121
	v_add3_u32 v116, 0, v103, v105
	v_lshlrev_b32_e32 v103, 1, v104
	v_lshrrev_b16_e32 v104, 1, v114
	v_lshrrev_b16_e32 v114, 1, v115
	v_lshrrev_b16_e32 v112, 1, v112
	v_add3_u32 v115, 0, v103, v105
	v_lshlrev_b32_e32 v103, 2, v104
	v_lshlrev_b32_e32 v104, 2, v114
	v_lshlrev_b32_e32 v112, 2, v112
	v_mov_b32_e32 v114, v235
	s_nop 0
	v_mov_b32_e32 v104, v236
	s_nop 0
	v_mov_b32_e32 v103, v237
	s_movk_i32 s0, 0x80
	v_cmp_gt_i32_e64 s[2:3], s1, v107
	s_waitcnt vmcnt(5)
	v_fma_mixlo_f16 v82, v82, v101, 0
	v_fma_mixlo_f16 v83, v83, v101, 0
	s_waitcnt vmcnt(4)
	v_fma_mixlo_f16 v70, v70, v102, 0
	v_fma_mixlo_f16 v66, v66, v102, 0
	v_fma_mixlo_f16 v84, v84, v101, 0
	v_fma_mixlo_f16 v85, v85, v101, 0
	v_fma_mixlo_f16 v86, v86, v101, 0
	v_fma_mixlo_f16 v87, v87, v101, 0
	v_fma_mixlo_f16 v88, v88, v101, 0
	v_fma_mixlo_f16 v89, v89, v101, 0
	v_fma_mixlo_f16 v90, v90, v101, 0
	v_fma_mixlo_f16 v91, v91, v101, 0
	v_fma_mixlo_f16 v92, v92, v101, 0
	v_fma_mixlo_f16 v93, v93, v101, 0
	v_fma_mixlo_f16 v94, v94, v101, 0
	v_fma_mixlo_f16 v95, v95, v101, 0
	v_fma_mixlo_f16 v96, v96, v101, 0
	v_fma_mixlo_f16 v97, v97, v101, 0
	ds_write_b16 v116, v82
	ds_write_b16 v116, v83 offset:384
	ds_write_b16 v116, v84 offset:768
	ds_write_b16 v116, v85 offset:1152
	ds_write_b16 v116, v86 offset:6144
	ds_write_b16 v116, v87 offset:6528
	ds_write_b16 v116, v88 offset:6912
	ds_write_b16 v116, v89 offset:7296
	ds_write_b16 v116, v90 offset:49152
	ds_write_b16 v116, v91 offset:49536
	ds_write_b16 v116, v92 offset:49920
	ds_write_b16 v116, v93 offset:50304
	ds_write_b16 v116, v94 offset:55296
	ds_write_b16 v116, v95 offset:55680
	ds_write_b16 v116, v96 offset:56064
	ds_write_b16 v116, v97 offset:56448
	v_fma_mixlo_f16 v71, v71, v102, 0
	v_fma_mixlo_f16 v72, v72, v102, 0
	v_fma_mixlo_f16 v73, v73, v102, 0
	v_fma_mixlo_f16 v67, v67, v102, 0
	v_fma_mixlo_f16 v68, v68, v102, 0
	ds_write_b16 v115, v70
	ds_write_b16 v115, v71 offset:384
	ds_write_b16 v115, v72 offset:768
	ds_write_b16 v115, v73 offset:1152
	ds_write_b16 v115, v66 offset:6144
	ds_write_b16 v115, v67 offset:6528
	ds_write_b16 v115, v68 offset:6912
	v_fma_mixlo_f16 v66, v69, v102, 0
	ds_write_b16 v115, v66 offset:7296
	v_fma_mixlo_f16 v66, v78, v102, 0
	ds_write_b16 v115, v66 offset:49152
	v_fma_mixlo_f16 v66, v79, v102, 0
	ds_write_b16 v115, v66 offset:49536
	v_fma_mixlo_f16 v66, v80, v102, 0
	ds_write_b16 v115, v66 offset:49920
	v_fma_mixlo_f16 v66, v81, v102, 0
	ds_write_b16 v115, v66 offset:50304
	v_fma_mixlo_f16 v66, v74, v102, 0
	ds_write_b16 v115, v66 offset:55296
	v_fma_mixlo_f16 v66, v75, v102, 0
	ds_write_b16 v115, v66 offset:55680
	v_fma_mixlo_f16 v66, v76, v102, 0
	ds_write_b16 v115, v66 offset:56064
	v_fma_mixlo_f16 v66, v77, v102, 0
	ds_write_b16 v115, v66 offset:56448
	v_xor_b32_e32 v66, v108, v124
	v_lshlrev_b32_e32 v66, 1, v66
	v_add3_u32 v66, 0, v66, v105
	s_waitcnt vmcnt(3)
	v_fma_mixlo_f16 v42, v42, v113, 0
	ds_write_b16 v66, v42 offset:6144
	v_fma_mixlo_f16 v42, v43, v113, 0
	ds_write_b16 v66, v42 offset:6528
	v_fma_mixlo_f16 v42, v44, v113, 0
	ds_write_b16 v66, v42 offset:6912
	v_fma_mixlo_f16 v42, v45, v113, 0
	ds_write_b16 v66, v42 offset:7296
	v_fma_mixlo_f16 v42, v62, v113, 0
	ds_write_b16 v66, v42 offset:49152
	v_fma_mixlo_f16 v42, v63, v113, 0
	ds_write_b16 v66, v42 offset:49536
	v_fma_mixlo_f16 v42, v64, v113, 0
	ds_write_b16 v66, v42 offset:49920
	v_fma_mixlo_f16 v42, v65, v113, 0
	ds_write_b16 v66, v42 offset:50304
	v_fma_mixlo_f16 v42, v58, v113, 0
	ds_write_b16 v66, v42 offset:55296
	v_fma_mixlo_f16 v42, v59, v113, 0
	ds_write_b16 v66, v42 offset:55680
	v_fma_mixlo_f16 v42, v60, v113, 0
	ds_write_b16 v66, v42 offset:56064
	v_fma_mixlo_f16 v42, v61, v113, 0
	ds_write_b16 v66, v42 offset:56448
	v_xor_b32_e32 v42, v110, v124
	v_lshlrev_b32_e32 v42, 1, v42
	v_add3_u32 v42, 0, v42, v105
	s_waitcnt vmcnt(2)
	v_fma_mixlo_f16 v34, v34, v114, 0
	ds_write_b16 v42, v34 offset:6144
	v_fma_mixlo_f16 v34, v35, v114, 0
	ds_write_b16 v42, v34 offset:6528
	v_fma_mixlo_f16 v34, v36, v114, 0
	ds_write_b16 v42, v34 offset:6912
	v_fma_mixlo_f16 v34, v37, v114, 0
	ds_write_b16 v42, v34 offset:7296
	v_fma_mixlo_f16 v34, v54, v114, 0
	ds_write_b16 v42, v34 offset:49152
	v_fma_mixlo_f16 v34, v55, v114, 0
	ds_write_b16 v42, v34 offset:49536
	v_fma_mixlo_f16 v34, v56, v114, 0
	ds_write_b16 v42, v34 offset:49920
	v_fma_mixlo_f16 v34, v57, v114, 0
	ds_write_b16 v42, v34 offset:50304
	v_fma_mixlo_f16 v34, v50, v114, 0
	ds_write_b16 v42, v34 offset:55296
	v_fma_mixlo_f16 v34, v51, v114, 0
	ds_write_b16 v42, v34 offset:55680
	v_fma_mixlo_f16 v34, v52, v114, 0
	ds_write_b16 v42, v34 offset:56064
	v_fma_mixlo_f16 v34, v53, v114, 0
	ds_write_b16 v42, v34 offset:56448
	v_xor_b32_e32 v34, v111, v124
	v_lshlrev_b32_e32 v34, 1, v34
	v_add3_u32 v34, 0, v34, v105
	s_waitcnt vmcnt(1)
	v_fma_mixlo_f16 v18, v18, v104, 0
	ds_write_b16 v34, v18 offset:6144
	v_fma_mixlo_f16 v18, v19, v104, 0
	ds_write_b16 v34, v18 offset:6528
	v_fma_mixlo_f16 v18, v20, v104, 0
	ds_write_b16 v34, v18 offset:6912
	v_fma_mixlo_f16 v18, v21, v104, 0
	ds_write_b16 v34, v18 offset:7296
	v_fma_mixlo_f16 v18, v30, v104, 0
	ds_write_b16 v34, v18 offset:49152
	v_fma_mixlo_f16 v18, v31, v104, 0
	ds_write_b16 v34, v18 offset:49536
	v_fma_mixlo_f16 v18, v32, v104, 0
	ds_write_b16 v34, v18 offset:49920
	v_fma_mixlo_f16 v18, v33, v104, 0
	ds_write_b16 v34, v18 offset:50304
	v_fma_mixlo_f16 v18, v26, v104, 0
	ds_write_b16 v34, v18 offset:55296
	v_fma_mixlo_f16 v18, v27, v104, 0
	ds_write_b16 v34, v18 offset:55680
	v_fma_mixlo_f16 v18, v28, v104, 0
	ds_write_b16 v34, v18 offset:56064
	v_fma_mixlo_f16 v18, v29, v104, 0
	ds_write_b16 v34, v18 offset:56448
	v_bitop3_b32 v18, v100, v124, s0 bitop3:0x36
	v_lshlrev_b32_e32 v18, 1, v18
	v_add3_u32 v18, 0, v18, v105
	s_waitcnt vmcnt(0)
	v_fma_mixlo_f16 v2, v2, v103, 0
	ds_write_b16 v18, v2 offset:6144
	v_fma_mixlo_f16 v2, v3, v103, 0
	ds_write_b16 v18, v2 offset:6528
	v_fma_mixlo_f16 v2, v4, v103, 0
	ds_write_b16 v18, v2 offset:6912
	v_fma_mixlo_f16 v2, v5, v103, 0
	ds_write_b16 v18, v2 offset:7296
	v_fma_mixlo_f16 v2, v14, v103, 0
	ds_write_b16 v18, v2 offset:49152
	v_fma_mixlo_f16 v2, v15, v103, 0
	ds_write_b16 v18, v2 offset:49536
	v_fma_mixlo_f16 v2, v16, v103, 0
	ds_write_b16 v18, v2 offset:49920
	v_fma_mixlo_f16 v2, v17, v103, 0
	ds_write_b16 v18, v2 offset:50304
	v_fma_mixlo_f16 v2, v10, v103, 0
	ds_write_b16 v18, v2 offset:55296
	v_fma_mixlo_f16 v2, v11, v103, 0
	ds_write_b16 v18, v2 offset:55680
	v_fma_mixlo_f16 v2, v12, v103, 0
	v_fma_mixlo_f16 v46, v46, v113, 0
	ds_write_b16 v18, v2 offset:56064
	v_fma_mixlo_f16 v2, v13, v103, 0
	s_mov_b32 s0, 0x2aaaaaab
	ds_write_b16 v66, v46
	v_fma_mixlo_f16 v46, v47, v113, 0
	ds_write_b16 v18, v2 offset:56448
	v_mul_hi_i32 v2, v107, s0
	ds_write_b16 v66, v46 offset:384
	v_fma_mixlo_f16 v46, v48, v113, 0
	v_fma_mixlo_f16 v38, v38, v114, 0
	v_lshrrev_b32_e32 v3, 31, v2
	v_ashrrev_i32_e32 v2, 4, v2
	ds_write_b16 v66, v46 offset:768
	v_fma_mixlo_f16 v46, v49, v113, 0
	ds_write_b16 v42, v38
	v_fma_mixlo_f16 v38, v39, v114, 0
	v_fma_mixlo_f16 v22, v22, v104, 0
	v_fma_mixlo_f16 v6, v6, v103, 0
	v_add_u32_e32 v49, v2, v3
	s_movk_i32 s0, 0x60
	ds_write_b16 v42, v38 offset:384
	v_fma_mixlo_f16 v38, v40, v114, 0
	ds_write_b16 v34, v22
	v_fma_mixlo_f16 v22, v23, v104, 0
	ds_write_b16 v18, v6
	v_fma_mixlo_f16 v6, v7, v103, 0
	v_mul_lo_u32 v2, v49, s0
	ds_write_b16 v66, v46 offset:1152
	ds_write_b16 v42, v38 offset:768
	v_fma_mixlo_f16 v38, v41, v114, 0
	ds_write_b16 v34, v22 offset:384
	v_fma_mixlo_f16 v22, v24, v104, 0
	ds_write_b16 v18, v6 offset:384
	v_fma_mixlo_f16 v6, v8, v103, 0
	v_sub_u32_e32 v14, v107, v2
	v_lshrrev_b32_e32 v2, 1, v121
	s_movk_i32 s0, 0x5e80
	ds_write_b16 v42, v38 offset:1152
	ds_write_b16 v34, v22 offset:768
	v_fma_mixlo_f16 v22, v25, v104, 0
	ds_write_b16 v18, v6 offset:768
	v_fma_mixlo_f16 v6, v9, v103, 0
	v_add_u32_e32 v8, v14, v2
	v_mov_b32_e32 v7, 0
	v_lshlrev_b32_e32 v2, 2, v14
	v_mul_lo_u32 v3, v49, s0
	ds_write_b16 v34, v22 offset:1152
	ds_write_b16 v18, v6 offset:1152
	v_ashrrev_i32_e32 v9, 31, v8
	v_mul_lo_u32 v45, v49, s75
	v_xor_b32_e32 v48, 0x60, v2
	v_xor_b32_e32 v47, 64, v2
	v_xor_b32_e32 v46, 32, v2
	v_add3_u32 v44, v3, v123, 0
	v_mov_b32_e32 v6, v7
	v_mov_b32_e32 v3, v7
	v_mov_b32_e32 v4, v7
	s_waitcnt lgkmcnt(0)
	s_barrier
	s_and_saveexec_b64 s[0:1], s[2:3]
	s_cbranch_execz .LBB1_73
	v_readlane_b32 s4, v230, 2
	v_readlane_b32 s5, v230, 3
	v_mov_b32_e32 v12, 0
	v_mov_b32_e32 v13, v12
	v_mov_b32_e32 v2, v240
	v_mov_b32_e32 v3, v241
	v_mov_b32_e32 v6, v242
	v_mov_b32_e32 v7, v243
	v_readlane_b32 s4, v230, 10
	v_readlane_b32 s6, v230, 4
	v_readlane_b32 s7, v230, 5
	v_add3_u32 v15, v45, v48, s4
	s_add_i32 s4, 0, 0xc00
	v_add3_u32 v16, v45, v47, s4
	s_add_i32 s4, 0, 0x600
	v_add3_u32 v17, v45, v46, s4
	v_mov_b32_e32 v26, v44
	v_add_u32_e32 v27, 0x200, v44
	v_mov_b32_e32 v28, v17
	v_add_u32_e32 v29, 0x200, v17
	v_mov_b32_e32 v30, v16
	v_add_u32_e32 v31, 0x200, v16
	v_mov_b32_e32 v32, v15
	v_add_u32_e32 v33, 0x200, v15
	ds_read2_b32 v[50:51], v26 offset1:96
	ds_read2_b32 v[52:53], v27 offset0:64 offset1:160
	ds_read2_b32 v[54:55], v28 offset1:96
	ds_read2_b32 v[56:57], v29 offset0:64 offset1:160
	v_add_u32_e32 v26, 0x1800, v26
	v_add_u32_e32 v27, 0x1800, v27
	v_add_u32_e32 v28, 0x1800, v28
	v_add_u32_e32 v29, 0x1800, v29
	ds_read2_b32 v[58:59], v30 offset1:96
	ds_read2_b32 v[60:61], v31 offset0:64 offset1:160
	ds_read2_b32 v[62:63], v32 offset1:96
	ds_read2_b32 v[64:65], v33 offset0:64 offset1:160
	v_add_u32_e32 v30, 0x1800, v30
	v_add_u32_e32 v31, 0x1800, v31
	v_add_u32_e32 v32, 0x1800, v32
	v_add_u32_e32 v33, 0x1800, v33
	ds_read2_b32 v[66:67], v26 offset1:96
	ds_read2_b32 v[68:69], v27 offset0:64 offset1:160
	ds_read2_b32 v[70:71], v28 offset1:96
	ds_read2_b32 v[72:73], v29 offset0:64 offset1:160
	v_add_u32_e32 v26, 0x1800, v26
	v_add_u32_e32 v27, 0x1800, v27
	v_add_u32_e32 v28, 0x1800, v28
	v_add_u32_e32 v29, 0x1800, v29
	s_waitcnt vmcnt(1)
	v_xor_b32_e32 v4, 0x80000000, v3
	v_mov_b32_e32 v10, v2
	v_mov_b32_e32 v11, v2
	v_mov_b32_e32 v5, v3
	s_waitcnt lgkmcnt(8)
	v_cvt_f32_f16_e32 v74, v50
	v_cvt_f32_f16_sdwa v75, v50 dst_sel:DWORD dst_unused:UNUSED_PAD src0_sel:WORD_1
	v_cvt_f32_f16_e32 v76, v51
	v_cvt_f32_f16_sdwa v77, v51 dst_sel:DWORD dst_unused:UNUSED_PAD src0_sel:WORD_1
	v_cvt_f32_f16_e32 v78, v52
	v_cvt_f32_f16_sdwa v79, v52 dst_sel:DWORD dst_unused:UNUSED_PAD src0_sel:WORD_1
	v_cvt_f32_f16_e32 v80, v53
	v_cvt_f32_f16_sdwa v81, v53 dst_sel:DWORD dst_unused:UNUSED_PAD src0_sel:WORD_1
	v_cvt_f32_f16_e32 v82, v54
	v_cvt_f32_f16_sdwa v83, v54 dst_sel:DWORD dst_unused:UNUSED_PAD src0_sel:WORD_1
	v_cvt_f32_f16_e32 v84, v55
	v_cvt_f32_f16_sdwa v85, v55 dst_sel:DWORD dst_unused:UNUSED_PAD src0_sel:WORD_1
	v_cvt_f32_f16_e32 v86, v56
	v_cvt_f32_f16_sdwa v87, v56 dst_sel:DWORD dst_unused:UNUSED_PAD src0_sel:WORD_1
	v_cvt_f32_f16_e32 v88, v57
	v_cvt_f32_f16_sdwa v89, v57 dst_sel:DWORD dst_unused:UNUSED_PAD src0_sel:WORD_1
	ds_read2_b32 v[50:51], v30 offset1:96
	ds_read2_b32 v[52:53], v31 offset0:64 offset1:160
	ds_read2_b32 v[54:55], v32 offset1:96
	ds_read2_b32 v[56:57], v33 offset0:64 offset1:160
	v_add_u32_e32 v30, 0x1800, v30
	v_add_u32_e32 v31, 0x1800, v31
	v_add_u32_e32 v32, 0x1800, v32
	v_add_u32_e32 v33, 0x1800, v33
	s_waitcnt lgkmcnt(8)
	v_pk_fma_f32 v[74:75], v[4:5], v[12:13], v[74:75] op_sel:[0,1,0] op_sel_hi:[1,0,1]
	v_cvt_f32_f16_e32 v90, v58
	v_pk_fma_f32 v[12:13], v[10:11], v[12:13], v[74:75]
	v_cvt_f32_f16_sdwa v91, v58 dst_sel:DWORD dst_unused:UNUSED_PAD src0_sel:WORD_1
	v_pk_fma_f32 v[76:77], v[4:5], v[12:13], v[76:77] op_sel:[0,1,0] op_sel_hi:[1,0,1]
	v_cvt_f32_f16_e32 v92, v59
	v_pk_fma_f32 v[12:13], v[10:11], v[12:13], v[76:77]
	v_cvt_f32_f16_sdwa v93, v59 dst_sel:DWORD dst_unused:UNUSED_PAD src0_sel:WORD_1
	v_pk_fma_f32 v[78:79], v[4:5], v[12:13], v[78:79] op_sel:[0,1,0] op_sel_hi:[1,0,1]
	v_cvt_f32_f16_e32 v94, v60
	v_pk_fma_f32 v[12:13], v[10:11], v[12:13], v[78:79]
	v_cvt_f32_f16_sdwa v95, v60 dst_sel:DWORD dst_unused:UNUSED_PAD src0_sel:WORD_1
	v_pk_fma_f32 v[80:81], v[4:5], v[12:13], v[80:81] op_sel:[0,1,0] op_sel_hi:[1,0,1]
	v_cvt_f32_f16_e32 v96, v61
	v_pk_fma_f32 v[12:13], v[10:11], v[12:13], v[80:81]
	v_cvt_f32_f16_sdwa v97, v61 dst_sel:DWORD dst_unused:UNUSED_PAD src0_sel:WORD_1
	v_pk_fma_f32 v[82:83], v[4:5], v[12:13], v[82:83] op_sel:[0,1,0] op_sel_hi:[1,0,1]
	v_cvt_f32_f16_e32 v18, v62
	v_pk_fma_f32 v[12:13], v[10:11], v[12:13], v[82:83]
	v_cvt_f32_f16_sdwa v19, v62 dst_sel:DWORD dst_unused:UNUSED_PAD src0_sel:WORD_1
	v_pk_fma_f32 v[84:85], v[4:5], v[12:13], v[84:85] op_sel:[0,1,0] op_sel_hi:[1,0,1]
	v_cvt_f32_f16_e32 v20, v63
	v_pk_fma_f32 v[12:13], v[10:11], v[12:13], v[84:85]
	v_cvt_f32_f16_sdwa v21, v63 dst_sel:DWORD dst_unused:UNUSED_PAD src0_sel:WORD_1
	v_pk_fma_f32 v[86:87], v[4:5], v[12:13], v[86:87] op_sel:[0,1,0] op_sel_hi:[1,0,1]
	v_cvt_f32_f16_e32 v22, v64
	v_pk_fma_f32 v[12:13], v[10:11], v[12:13], v[86:87]
	v_cvt_f32_f16_sdwa v23, v64 dst_sel:DWORD dst_unused:UNUSED_PAD src0_sel:WORD_1
	v_pk_fma_f32 v[88:89], v[4:5], v[12:13], v[88:89] op_sel:[0,1,0] op_sel_hi:[1,0,1]
	v_cvt_f32_f16_e32 v24, v65
	v_pk_fma_f32 v[12:13], v[10:11], v[12:13], v[88:89]
	v_cvt_f32_f16_sdwa v25, v65 dst_sel:DWORD dst_unused:UNUSED_PAD src0_sel:WORD_1
	ds_read2_b32 v[58:59], v26 offset1:96
	ds_read2_b32 v[60:61], v27 offset0:64 offset1:160
	ds_read2_b32 v[62:63], v28 offset1:96
	ds_read2_b32 v[64:65], v29 offset0:64 offset1:160
	v_add_u32_e32 v26, 0x1800, v26
	v_add_u32_e32 v27, 0x1800, v27
	v_add_u32_e32 v28, 0x1800, v28
	v_add_u32_e32 v29, 0x1800, v29
	s_waitcnt lgkmcnt(8)
	v_pk_fma_f32 v[90:91], v[4:5], v[12:13], v[90:91] op_sel:[0,1,0] op_sel_hi:[1,0,1]
	v_cvt_f32_f16_e32 v74, v66
	v_pk_fma_f32 v[12:13], v[10:11], v[12:13], v[90:91]
	v_cvt_f32_f16_sdwa v75, v66 dst_sel:DWORD dst_unused:UNUSED_PAD src0_sel:WORD_1
	v_pk_fma_f32 v[92:93], v[4:5], v[12:13], v[92:93] op_sel:[0,1,0] op_sel_hi:[1,0,1]
	v_cvt_f32_f16_e32 v76, v67
	v_pk_fma_f32 v[12:13], v[10:11], v[12:13], v[92:93]
	v_cvt_f32_f16_sdwa v77, v67 dst_sel:DWORD dst_unused:UNUSED_PAD src0_sel:WORD_1
	v_pk_fma_f32 v[94:95], v[4:5], v[12:13], v[94:95] op_sel:[0,1,0] op_sel_hi:[1,0,1]
	v_cvt_f32_f16_e32 v78, v68
	v_pk_fma_f32 v[12:13], v[10:11], v[12:13], v[94:95]
	v_cvt_f32_f16_sdwa v79, v68 dst_sel:DWORD dst_unused:UNUSED_PAD src0_sel:WORD_1
	v_pk_fma_f32 v[96:97], v[4:5], v[12:13], v[96:97] op_sel:[0,1,0] op_sel_hi:[1,0,1]
	v_cvt_f32_f16_e32 v80, v69
	v_pk_fma_f32 v[12:13], v[10:11], v[12:13], v[96:97]
	v_cvt_f32_f16_sdwa v81, v69 dst_sel:DWORD dst_unused:UNUSED_PAD src0_sel:WORD_1
	v_pk_fma_f32 v[18:19], v[4:5], v[12:13], v[18:19] op_sel:[0,1,0] op_sel_hi:[1,0,1]
	v_cvt_f32_f16_e32 v82, v70
	v_pk_fma_f32 v[12:13], v[10:11], v[12:13], v[18:19]
	v_cvt_f32_f16_sdwa v83, v70 dst_sel:DWORD dst_unused:UNUSED_PAD src0_sel:WORD_1
	v_pk_fma_f32 v[20:21], v[4:5], v[12:13], v[20:21] op_sel:[0,1,0] op_sel_hi:[1,0,1]
	v_cvt_f32_f16_e32 v84, v71
	v_pk_fma_f32 v[12:13], v[10:11], v[12:13], v[20:21]
	v_cvt_f32_f16_sdwa v85, v71 dst_sel:DWORD dst_unused:UNUSED_PAD src0_sel:WORD_1
	v_pk_fma_f32 v[22:23], v[4:5], v[12:13], v[22:23] op_sel:[0,1,0] op_sel_hi:[1,0,1]
	v_cvt_f32_f16_e32 v86, v72
	v_pk_fma_f32 v[12:13], v[10:11], v[12:13], v[22:23]
	v_cvt_f32_f16_sdwa v87, v72 dst_sel:DWORD dst_unused:UNUSED_PAD src0_sel:WORD_1
	v_pk_fma_f32 v[24:25], v[4:5], v[12:13], v[24:25] op_sel:[0,1,0] op_sel_hi:[1,0,1]
	v_cvt_f32_f16_e32 v88, v73
	v_pk_fma_f32 v[12:13], v[10:11], v[12:13], v[24:25]
	v_cvt_f32_f16_sdwa v89, v73 dst_sel:DWORD dst_unused:UNUSED_PAD src0_sel:WORD_1
	ds_read2_b32 v[66:67], v30 offset1:96
	ds_read2_b32 v[68:69], v31 offset0:64 offset1:160
	ds_read2_b32 v[70:71], v32 offset1:96
	ds_read2_b32 v[72:73], v33 offset0:64 offset1:160
	v_add_u32_e32 v30, 0x1800, v30
	v_add_u32_e32 v31, 0x1800, v31
	v_add_u32_e32 v32, 0x1800, v32
	v_add_u32_e32 v33, 0x1800, v33
	s_waitcnt lgkmcnt(8)
	v_pk_fma_f32 v[74:75], v[4:5], v[12:13], v[74:75] op_sel:[0,1,0] op_sel_hi:[1,0,1]
	v_cvt_f32_f16_e32 v90, v50
	v_pk_fma_f32 v[12:13], v[10:11], v[12:13], v[74:75]
	v_cvt_f32_f16_sdwa v91, v50 dst_sel:DWORD dst_unused:UNUSED_PAD src0_sel:WORD_1
	v_pk_fma_f32 v[76:77], v[4:5], v[12:13], v[76:77] op_sel:[0,1,0] op_sel_hi:[1,0,1]
	v_cvt_f32_f16_e32 v92, v51
	v_pk_fma_f32 v[12:13], v[10:11], v[12:13], v[76:77]
	v_cvt_f32_f16_sdwa v93, v51 dst_sel:DWORD dst_unused:UNUSED_PAD src0_sel:WORD_1
	v_pk_fma_f32 v[78:79], v[4:5], v[12:13], v[78:79] op_sel:[0,1,0] op_sel_hi:[1,0,1]
	v_cvt_f32_f16_e32 v94, v52
	v_pk_fma_f32 v[12:13], v[10:11], v[12:13], v[78:79]
	v_cvt_f32_f16_sdwa v95, v52 dst_sel:DWORD dst_unused:UNUSED_PAD src0_sel:WORD_1
	v_pk_fma_f32 v[80:81], v[4:5], v[12:13], v[80:81] op_sel:[0,1,0] op_sel_hi:[1,0,1]
	v_cvt_f32_f16_e32 v96, v53
	v_pk_fma_f32 v[12:13], v[10:11], v[12:13], v[80:81]
	v_cvt_f32_f16_sdwa v97, v53 dst_sel:DWORD dst_unused:UNUSED_PAD src0_sel:WORD_1
	v_pk_fma_f32 v[82:83], v[4:5], v[12:13], v[82:83] op_sel:[0,1,0] op_sel_hi:[1,0,1]
	v_cvt_f32_f16_e32 v18, v54
	v_pk_fma_f32 v[12:13], v[10:11], v[12:13], v[82:83]
	v_cvt_f32_f16_sdwa v19, v54 dst_sel:DWORD dst_unused:UNUSED_PAD src0_sel:WORD_1
	v_pk_fma_f32 v[84:85], v[4:5], v[12:13], v[84:85] op_sel:[0,1,0] op_sel_hi:[1,0,1]
	v_cvt_f32_f16_e32 v20, v55
	v_pk_fma_f32 v[12:13], v[10:11], v[12:13], v[84:85]
	v_cvt_f32_f16_sdwa v21, v55 dst_sel:DWORD dst_unused:UNUSED_PAD src0_sel:WORD_1
	v_pk_fma_f32 v[86:87], v[4:5], v[12:13], v[86:87] op_sel:[0,1,0] op_sel_hi:[1,0,1]
	v_cvt_f32_f16_e32 v22, v56
	v_pk_fma_f32 v[12:13], v[10:11], v[12:13], v[86:87]
	v_cvt_f32_f16_sdwa v23, v56 dst_sel:DWORD dst_unused:UNUSED_PAD src0_sel:WORD_1
	v_pk_fma_f32 v[88:89], v[4:5], v[12:13], v[88:89] op_sel:[0,1,0] op_sel_hi:[1,0,1]
	v_cvt_f32_f16_e32 v24, v57
	v_pk_fma_f32 v[12:13], v[10:11], v[12:13], v[88:89]
	v_cvt_f32_f16_sdwa v25, v57 dst_sel:DWORD dst_unused:UNUSED_PAD src0_sel:WORD_1
	ds_read2_b32 v[50:51], v26 offset1:96
	ds_read2_b32 v[52:53], v27 offset0:64 offset1:160
	ds_read2_b32 v[54:55], v28 offset1:96
	ds_read2_b32 v[56:57], v29 offset0:64 offset1:160
	v_add_u32_e32 v26, 0x1800, v26
	v_add_u32_e32 v27, 0x1800, v27
	v_add_u32_e32 v28, 0x1800, v28
	v_add_u32_e32 v29, 0x1800, v29
	s_waitcnt lgkmcnt(8)
	v_pk_fma_f32 v[90:91], v[4:5], v[12:13], v[90:91] op_sel:[0,1,0] op_sel_hi:[1,0,1]
	v_cvt_f32_f16_e32 v74, v58
	v_pk_fma_f32 v[12:13], v[10:11], v[12:13], v[90:91]
	v_cvt_f32_f16_sdwa v75, v58 dst_sel:DWORD dst_unused:UNUSED_PAD src0_sel:WORD_1
	v_pk_fma_f32 v[92:93], v[4:5], v[12:13], v[92:93] op_sel:[0,1,0] op_sel_hi:[1,0,1]
	v_cvt_f32_f16_e32 v76, v59
	v_pk_fma_f32 v[12:13], v[10:11], v[12:13], v[92:93]
	v_cvt_f32_f16_sdwa v77, v59 dst_sel:DWORD dst_unused:UNUSED_PAD src0_sel:WORD_1
	v_pk_fma_f32 v[94:95], v[4:5], v[12:13], v[94:95] op_sel:[0,1,0] op_sel_hi:[1,0,1]
	v_cvt_f32_f16_e32 v78, v60
	v_pk_fma_f32 v[12:13], v[10:11], v[12:13], v[94:95]
	v_cvt_f32_f16_sdwa v79, v60 dst_sel:DWORD dst_unused:UNUSED_PAD src0_sel:WORD_1
	v_pk_fma_f32 v[96:97], v[4:5], v[12:13], v[96:97] op_sel:[0,1,0] op_sel_hi:[1,0,1]
	v_cvt_f32_f16_e32 v80, v61
	v_pk_fma_f32 v[12:13], v[10:11], v[12:13], v[96:97]
	v_cvt_f32_f16_sdwa v81, v61 dst_sel:DWORD dst_unused:UNUSED_PAD src0_sel:WORD_1
	v_pk_fma_f32 v[18:19], v[4:5], v[12:13], v[18:19] op_sel:[0,1,0] op_sel_hi:[1,0,1]
	v_cvt_f32_f16_e32 v82, v62
	v_pk_fma_f32 v[12:13], v[10:11], v[12:13], v[18:19]
	v_cvt_f32_f16_sdwa v83, v62 dst_sel:DWORD dst_unused:UNUSED_PAD src0_sel:WORD_1
	v_pk_fma_f32 v[20:21], v[4:5], v[12:13], v[20:21] op_sel:[0,1,0] op_sel_hi:[1,0,1]
	v_cvt_f32_f16_e32 v84, v63
	v_pk_fma_f32 v[12:13], v[10:11], v[12:13], v[20:21]
	v_cvt_f32_f16_sdwa v85, v63 dst_sel:DWORD dst_unused:UNUSED_PAD src0_sel:WORD_1
	v_pk_fma_f32 v[22:23], v[4:5], v[12:13], v[22:23] op_sel:[0,1,0] op_sel_hi:[1,0,1]
	v_cvt_f32_f16_e32 v86, v64
	v_pk_fma_f32 v[12:13], v[10:11], v[12:13], v[22:23]
	v_cvt_f32_f16_sdwa v87, v64 dst_sel:DWORD dst_unused:UNUSED_PAD src0_sel:WORD_1
	v_pk_fma_f32 v[24:25], v[4:5], v[12:13], v[24:25] op_sel:[0,1,0] op_sel_hi:[1,0,1]
	v_cvt_f32_f16_e32 v88, v65
	v_pk_fma_f32 v[12:13], v[10:11], v[12:13], v[24:25]
	v_cvt_f32_f16_sdwa v89, v65 dst_sel:DWORD dst_unused:UNUSED_PAD src0_sel:WORD_1
	ds_read2_b32 v[58:59], v30 offset1:96
	ds_read2_b32 v[60:61], v31 offset0:64 offset1:160
	ds_read2_b32 v[62:63], v32 offset1:96
	ds_read2_b32 v[64:65], v33 offset0:64 offset1:160
	v_add_u32_e32 v30, 0x1800, v30
	v_add_u32_e32 v31, 0x1800, v31
	v_add_u32_e32 v32, 0x1800, v32
	v_add_u32_e32 v33, 0x1800, v33
	s_waitcnt lgkmcnt(8)
	v_pk_fma_f32 v[74:75], v[4:5], v[12:13], v[74:75] op_sel:[0,1,0] op_sel_hi:[1,0,1]
	v_cvt_f32_f16_e32 v90, v66
	v_pk_fma_f32 v[12:13], v[10:11], v[12:13], v[74:75]
	v_cvt_f32_f16_sdwa v91, v66 dst_sel:DWORD dst_unused:UNUSED_PAD src0_sel:WORD_1
	v_pk_fma_f32 v[76:77], v[4:5], v[12:13], v[76:77] op_sel:[0,1,0] op_sel_hi:[1,0,1]
	v_cvt_f32_f16_e32 v92, v67
	v_pk_fma_f32 v[12:13], v[10:11], v[12:13], v[76:77]
	v_cvt_f32_f16_sdwa v93, v67 dst_sel:DWORD dst_unused:UNUSED_PAD src0_sel:WORD_1
	v_pk_fma_f32 v[78:79], v[4:5], v[12:13], v[78:79] op_sel:[0,1,0] op_sel_hi:[1,0,1]
	v_cvt_f32_f16_e32 v94, v68
	v_pk_fma_f32 v[12:13], v[10:11], v[12:13], v[78:79]
	v_cvt_f32_f16_sdwa v95, v68 dst_sel:DWORD dst_unused:UNUSED_PAD src0_sel:WORD_1
	v_pk_fma_f32 v[80:81], v[4:5], v[12:13], v[80:81] op_sel:[0,1,0] op_sel_hi:[1,0,1]
	v_cvt_f32_f16_e32 v96, v69
	v_pk_fma_f32 v[12:13], v[10:11], v[12:13], v[80:81]
	v_cvt_f32_f16_sdwa v97, v69 dst_sel:DWORD dst_unused:UNUSED_PAD src0_sel:WORD_1
	v_pk_fma_f32 v[82:83], v[4:5], v[12:13], v[82:83] op_sel:[0,1,0] op_sel_hi:[1,0,1]
	v_cvt_f32_f16_e32 v18, v70
	v_pk_fma_f32 v[12:13], v[10:11], v[12:13], v[82:83]
	v_cvt_f32_f16_sdwa v19, v70 dst_sel:DWORD dst_unused:UNUSED_PAD src0_sel:WORD_1
	v_pk_fma_f32 v[84:85], v[4:5], v[12:13], v[84:85] op_sel:[0,1,0] op_sel_hi:[1,0,1]
	v_cvt_f32_f16_e32 v20, v71
	v_pk_fma_f32 v[12:13], v[10:11], v[12:13], v[84:85]
	v_cvt_f32_f16_sdwa v21, v71 dst_sel:DWORD dst_unused:UNUSED_PAD src0_sel:WORD_1
	v_pk_fma_f32 v[86:87], v[4:5], v[12:13], v[86:87] op_sel:[0,1,0] op_sel_hi:[1,0,1]
	v_cvt_f32_f16_e32 v22, v72
	v_pk_fma_f32 v[12:13], v[10:11], v[12:13], v[86:87]
	v_cvt_f32_f16_sdwa v23, v72 dst_sel:DWORD dst_unused:UNUSED_PAD src0_sel:WORD_1
	v_pk_fma_f32 v[88:89], v[4:5], v[12:13], v[88:89] op_sel:[0,1,0] op_sel_hi:[1,0,1]
	v_cvt_f32_f16_e32 v24, v73
	v_pk_fma_f32 v[12:13], v[10:11], v[12:13], v[88:89]
	v_cvt_f32_f16_sdwa v25, v73 dst_sel:DWORD dst_unused:UNUSED_PAD src0_sel:WORD_1
	s_waitcnt lgkmcnt(4)
	v_pk_fma_f32 v[90:91], v[4:5], v[12:13], v[90:91] op_sel:[0,1,0] op_sel_hi:[1,0,1]
	v_cvt_f32_f16_e32 v74, v50
	v_pk_fma_f32 v[12:13], v[10:11], v[12:13], v[90:91]
	v_cvt_f32_f16_sdwa v75, v50 dst_sel:DWORD dst_unused:UNUSED_PAD src0_sel:WORD_1
	v_pk_fma_f32 v[92:93], v[4:5], v[12:13], v[92:93] op_sel:[0,1,0] op_sel_hi:[1,0,1]
	v_cvt_f32_f16_e32 v76, v51
	v_pk_fma_f32 v[12:13], v[10:11], v[12:13], v[92:93]
	v_cvt_f32_f16_sdwa v77, v51 dst_sel:DWORD dst_unused:UNUSED_PAD src0_sel:WORD_1
	v_pk_fma_f32 v[94:95], v[4:5], v[12:13], v[94:95] op_sel:[0,1,0] op_sel_hi:[1,0,1]
	v_cvt_f32_f16_e32 v78, v52
	v_pk_fma_f32 v[12:13], v[10:11], v[12:13], v[94:95]
	v_cvt_f32_f16_sdwa v79, v52 dst_sel:DWORD dst_unused:UNUSED_PAD src0_sel:WORD_1
	v_pk_fma_f32 v[96:97], v[4:5], v[12:13], v[96:97] op_sel:[0,1,0] op_sel_hi:[1,0,1]
	v_cvt_f32_f16_e32 v80, v53
	v_pk_fma_f32 v[12:13], v[10:11], v[12:13], v[96:97]
	v_cvt_f32_f16_sdwa v81, v53 dst_sel:DWORD dst_unused:UNUSED_PAD src0_sel:WORD_1
	v_pk_fma_f32 v[18:19], v[4:5], v[12:13], v[18:19] op_sel:[0,1,0] op_sel_hi:[1,0,1]
	v_cvt_f32_f16_e32 v82, v54
	v_pk_fma_f32 v[12:13], v[10:11], v[12:13], v[18:19]
	v_cvt_f32_f16_sdwa v83, v54 dst_sel:DWORD dst_unused:UNUSED_PAD src0_sel:WORD_1
	v_pk_fma_f32 v[20:21], v[4:5], v[12:13], v[20:21] op_sel:[0,1,0] op_sel_hi:[1,0,1]
	v_cvt_f32_f16_e32 v84, v55
	v_pk_fma_f32 v[12:13], v[10:11], v[12:13], v[20:21]
	v_cvt_f32_f16_sdwa v85, v55 dst_sel:DWORD dst_unused:UNUSED_PAD src0_sel:WORD_1
	v_pk_fma_f32 v[22:23], v[4:5], v[12:13], v[22:23] op_sel:[0,1,0] op_sel_hi:[1,0,1]
	v_cvt_f32_f16_e32 v86, v56
	v_pk_fma_f32 v[12:13], v[10:11], v[12:13], v[22:23]
	v_cvt_f32_f16_sdwa v87, v56 dst_sel:DWORD dst_unused:UNUSED_PAD src0_sel:WORD_1
	v_pk_fma_f32 v[24:25], v[4:5], v[12:13], v[24:25] op_sel:[0,1,0] op_sel_hi:[1,0,1]
	v_cvt_f32_f16_e32 v88, v57
	v_pk_fma_f32 v[12:13], v[10:11], v[12:13], v[24:25]
	v_cvt_f32_f16_sdwa v89, v57 dst_sel:DWORD dst_unused:UNUSED_PAD src0_sel:WORD_1
	s_waitcnt lgkmcnt(0)
	v_pk_fma_f32 v[74:75], v[4:5], v[12:13], v[74:75] op_sel:[0,1,0] op_sel_hi:[1,0,1]
	v_cvt_f32_f16_e32 v90, v58
	v_pk_fma_f32 v[12:13], v[10:11], v[12:13], v[74:75]
	v_cvt_f32_f16_sdwa v91, v58 dst_sel:DWORD dst_unused:UNUSED_PAD src0_sel:WORD_1
	v_pk_fma_f32 v[76:77], v[4:5], v[12:13], v[76:77] op_sel:[0,1,0] op_sel_hi:[1,0,1]
	v_cvt_f32_f16_e32 v92, v59
	v_pk_fma_f32 v[12:13], v[10:11], v[12:13], v[76:77]
	v_cvt_f32_f16_sdwa v93, v59 dst_sel:DWORD dst_unused:UNUSED_PAD src0_sel:WORD_1
	v_pk_fma_f32 v[78:79], v[4:5], v[12:13], v[78:79] op_sel:[0,1,0] op_sel_hi:[1,0,1]
	v_cvt_f32_f16_e32 v94, v60
	v_pk_fma_f32 v[12:13], v[10:11], v[12:13], v[78:79]
	v_cvt_f32_f16_sdwa v95, v60 dst_sel:DWORD dst_unused:UNUSED_PAD src0_sel:WORD_1
	v_pk_fma_f32 v[80:81], v[4:5], v[12:13], v[80:81] op_sel:[0,1,0] op_sel_hi:[1,0,1]
	v_cvt_f32_f16_e32 v96, v61
	v_pk_fma_f32 v[12:13], v[10:11], v[12:13], v[80:81]
	v_cvt_f32_f16_sdwa v97, v61 dst_sel:DWORD dst_unused:UNUSED_PAD src0_sel:WORD_1
	v_pk_fma_f32 v[82:83], v[4:5], v[12:13], v[82:83] op_sel:[0,1,0] op_sel_hi:[1,0,1]
	v_cvt_f32_f16_e32 v18, v62
	v_pk_fma_f32 v[12:13], v[10:11], v[12:13], v[82:83]
	v_cvt_f32_f16_sdwa v19, v62 dst_sel:DWORD dst_unused:UNUSED_PAD src0_sel:WORD_1
	v_pk_fma_f32 v[84:85], v[4:5], v[12:13], v[84:85] op_sel:[0,1,0] op_sel_hi:[1,0,1]
	v_cvt_f32_f16_e32 v20, v63
	v_pk_fma_f32 v[12:13], v[10:11], v[12:13], v[84:85]
	v_cvt_f32_f16_sdwa v21, v63 dst_sel:DWORD dst_unused:UNUSED_PAD src0_sel:WORD_1
	v_pk_fma_f32 v[86:87], v[4:5], v[12:13], v[86:87] op_sel:[0,1,0] op_sel_hi:[1,0,1]
	v_cvt_f32_f16_e32 v22, v64
	v_pk_fma_f32 v[12:13], v[10:11], v[12:13], v[86:87]
	v_cvt_f32_f16_sdwa v23, v64 dst_sel:DWORD dst_unused:UNUSED_PAD src0_sel:WORD_1
	v_pk_fma_f32 v[88:89], v[4:5], v[12:13], v[88:89] op_sel:[0,1,0] op_sel_hi:[1,0,1]
	v_cvt_f32_f16_e32 v24, v65
	v_pk_fma_f32 v[12:13], v[10:11], v[12:13], v[88:89]
	v_cvt_f32_f16_sdwa v25, v65 dst_sel:DWORD dst_unused:UNUSED_PAD src0_sel:WORD_1
	v_pk_fma_f32 v[90:91], v[4:5], v[12:13], v[90:91] op_sel:[0,1,0] op_sel_hi:[1,0,1]
	s_nop 0
	v_pk_fma_f32 v[12:13], v[10:11], v[12:13], v[90:91]
	s_nop 0
	v_pk_fma_f32 v[92:93], v[4:5], v[12:13], v[92:93] op_sel:[0,1,0] op_sel_hi:[1,0,1]
	s_nop 0
	v_pk_fma_f32 v[12:13], v[10:11], v[12:13], v[92:93]
	s_nop 0
	v_pk_fma_f32 v[94:95], v[4:5], v[12:13], v[94:95] op_sel:[0,1,0] op_sel_hi:[1,0,1]
	s_nop 0
	v_pk_fma_f32 v[12:13], v[10:11], v[12:13], v[94:95]
	s_nop 0
	v_pk_fma_f32 v[96:97], v[4:5], v[12:13], v[96:97] op_sel:[0,1,0] op_sel_hi:[1,0,1]
	s_nop 0
	v_pk_fma_f32 v[12:13], v[10:11], v[12:13], v[96:97]
	s_nop 0
	v_pk_fma_f32 v[18:19], v[4:5], v[12:13], v[18:19] op_sel:[0,1,0] op_sel_hi:[1,0,1]
	s_nop 0
	v_pk_fma_f32 v[12:13], v[10:11], v[12:13], v[18:19]
	s_nop 0
	v_pk_fma_f32 v[20:21], v[4:5], v[12:13], v[20:21] op_sel:[0,1,0] op_sel_hi:[1,0,1]
	s_nop 0
	v_pk_fma_f32 v[12:13], v[10:11], v[12:13], v[20:21]
	s_nop 0
	v_pk_fma_f32 v[22:23], v[4:5], v[12:13], v[22:23] op_sel:[0,1,0] op_sel_hi:[1,0,1]
	s_nop 0
	v_pk_fma_f32 v[12:13], v[10:11], v[12:13], v[22:23]
	s_nop 0
	v_pk_fma_f32 v[24:25], v[4:5], v[12:13], v[24:25] op_sel:[0,1,0] op_sel_hi:[1,0,1]
	s_nop 0
	v_pk_fma_f32 v[12:13], v[10:11], v[12:13], v[24:25]
	s_nop 0
	v_mul_lo_u32 v4, v49, s67
	v_lshlrev_b32_e32 v5, 3, v14
	v_readlane_b32 s4, v230, 8
	s_nop 1
	v_add3_u32 v4, s4, v4, v5
	ds_write_b64 v4, v[12:13]
	v_mov_b32_e32 v4, v2

.LBB1_208:
	s_or_b64 exec, exec, s[0:1]
	v_and_b32_e32 v15, 63, v107
	v_ashrrev_i32_e32 v2, 6, v107
	v_mul_lo_u16_e32 v4, 0xab, v15
	v_lshlrev_b32_e32 v14, 5, v2
	v_lshrrev_b16_e32 v4, 12, v4
	v_or_b32_e32 v8, v14, v4
	v_lshlrev_b16_e32 v4, 3, v4
	v_add_u16_e32 v4, v107, v4
	v_lshlrev_b32_e32 v108, 1, v121
	s_movk_i32 s2, 0x180
	v_lshlrev_b16_e32 v4, 3, v4
	v_lshl_add_u64 v[2:3], s[44:45], 0, v[108:109]
	v_mul_lo_u32 v5, v8, s2
	v_and_b32_e32 v4, 0xf8, v4
	v_add_u32_e32 v8, v8, v120
	v_lshlrev_b32_e32 v108, 1, v4
	v_mad_i64_i32 v[8:9], s[0:1], v8, s56, v[2:3]
	v_lshl_add_u64 v[12:13], v[8:9], 0, v[108:109]
	v_bitop3_b16 v8, v107, 64, 63 bitop3:0xec
	v_mul_lo_u16_e32 v8, 0xab, v8
	v_lshrrev_b16_e32 v8, 12, v8
	v_lshlrev_b16_e32 v9, 3, v8
	v_add_u16_e32 v9, v107, v9
	v_lshlrev_b16_e32 v9, 3, v9
	v_add3_u32 v4, 0, v5, v108
	v_or_b32_e32 v16, v14, v8
	v_and_b32_e32 v17, 0xf8, v9
	v_lshlrev_b32_e32 v8, 2, v8
	s_waitcnt lgkmcnt(0)
	s_barrier
	s_waitcnt vmcnt(0)
	s_and_saveexec_b64 s[100:101], s[34:35]
	s_cbranch_execz .Lpf_skip_g1
	v_readfirstlane_b32 s10, v173
	s_lshl_b32 s10, s10, 7
	s_add_u32 s10, s64, s10
	s_addc_u32 s11, s65, 0
	global_atomic_add v231, v109, v1, s[10:11] sc0

	.amdhsa_kernel _Z11mega_kernelPKfPDF16_PKDF16_S3_S1_PfS0_S0_PK15HIP_vector_typeIfLj2EEPS6_
		.amdhsa_group_segment_fixed_size 0
		.amdhsa_private_segment_fixed_size 0
		.amdhsa_kernarg_size 80
		.amdhsa_user_sgpr_count 2
		.amdhsa_user_sgpr_dispatch_ptr 0
		.amdhsa_user_sgpr_queue_ptr 0
		.amdhsa_user_sgpr_kernarg_segment_ptr 1
		.amdhsa_user_sgpr_dispatch_id 0
		.amdhsa_user_sgpr_kernarg_preload_length 0
		.amdhsa_user_sgpr_kernarg_preload_offset 0
		.amdhsa_user_sgpr_private_segment_size 0
		.amdhsa_uses_dynamic_stack 0
		.amdhsa_enable_private_segment 0
		.amdhsa_system_sgpr_workgroup_id_x 1
		.amdhsa_system_sgpr_workgroup_id_y 0
		.amdhsa_system_sgpr_workgroup_id_z 0
		.amdhsa_system_sgpr_workgroup_info 0
		.amdhsa_system_vgpr_workitem_id 0
		.amdhsa_next_free_vgpr 256
		.amdhsa_next_free_sgpr 102
		.amdhsa_accum_offset 256
		.amdhsa_reserve_vcc 1
		.amdhsa_float_round_mode_32 0
		.amdhsa_float_round_mode_16_64 0
		.amdhsa_float_denorm_mode_32 3
		.amdhsa_float_denorm_mode_16_64 3
		.amdhsa_dx10_clamp 1
		.amdhsa_ieee_mode 1
		.amdhsa_fp16_overflow 0
		.amdhsa_tg_split 0
		.amdhsa_exception_fp_ieee_invalid_op 0
		.amdhsa_exception_fp_denorm_src 0
		.amdhsa_exception_fp_ieee_div_zero 0
		.amdhsa_exception_fp_ieee_overflow 0
		.amdhsa_exception_fp_ieee_underflow 0
		.amdhsa_exception_fp_ieee_inexact 0
		.amdhsa_exception_int_div_zero 0
	.end_amdhsa_kernel

amdhsa.kernels:
  - .agpr_count:     0
    .args:
      - .actual_access:  read_only
        .address_space:  global
        .offset:         0
        .size:           8
        .value_kind:     global_buffer
      - .actual_access:  write_only
        .address_space:  global
        .offset:         8
        .size:           8
        .value_kind:     global_buffer
      - .offset:         16
        .size:           8
        .value_kind:     by_value
      - .actual_access:  read_only
        .address_space:  global
        .offset:         24
        .size:           8
        .value_kind:     global_buffer
      - .actual_access:  read_only
        .address_space:  global
        .offset:         32
        .size:           8
        .value_kind:     global_buffer
      - .actual_access:  read_only
        .address_space:  global
        .offset:         40
        .size:           8
        .value_kind:     global_buffer
      - .actual_access:  read_only
        .address_space:  global
        .offset:         48
        .size:           8
        .value_kind:     global_buffer
      - .actual_access:  read_only
        .address_space:  global
        .offset:         56
        .size:           8
        .value_kind:     global_buffer
      - .actual_access:  write_only
        .address_space:  global
        .offset:         64
        .size:           8
        .value_kind:     global_buffer
      - .actual_access:  write_only
        .address_space:  global
        .offset:         72
        .size:           8
        .value_kind:     global_buffer
      - .actual_access:  write_only
        .address_space:  global
        .offset:         80
        .size:           8
        .value_kind:     global_buffer
      - .actual_access:  write_only
        .address_space:  global
        .offset:         88
        .size:           8
        .value_kind:     global_buffer
      - .actual_access:  write_only
        .address_space:  global
        .offset:         96
        .size:           8
        .value_kind:     global_buffer
      - .actual_access:  write_only
        .address_space:  global
        .offset:         104
        .size:           8
        .value_kind:     global_buffer
    .group_segment_fixed_size: 0
    .kernarg_segment_align: 8
    .kernarg_segment_size: 112
    .language:       OpenCL C
    .language_version:
      - 2
      - 0
    .max_flat_workgroup_size: 256
    .name:           _Z15prep_cvt_kernelPKfPDF16_mS0_S0_S0_S0_S0_S1_S1_P15HIP_vector_typeIfLj2EEPfS4_Py
    .private_segment_fixed_size: 0
    .sgpr_count:     22
    .sgpr_spill_count: 0
    .symbol:         _Z15prep_cvt_kernelPKfPDF16_mS0_S0_S0_S0_S0_S1_S1_P15HIP_vector_typeIfLj2EEPfS4_Py.kd
    .uniform_work_group_size: 1
    .uses_dynamic_stack: false
    .vgpr_count:     25
    .vgpr_spill_count: 0
    .wavefront_size: 64
  - .agpr_count:     0
    .args:
      - .actual_access:  read_only
        .address_space:  global
        .offset:         0
        .size:           8
        .value_kind:     global_buffer
      - .address_space:  global
        .offset:         8
        .size:           8
        .value_kind:     global_buffer
      - .address_space:  global
        .offset:         16
        .size:           8
        .value_kind:     global_buffer
      - .address_space:  global
        .offset:         24
        .size:           8
        .value_kind:     global_buffer
      - .address_space:  global
        .offset:         32
        .size:           8
        .value_kind:     global_buffer
      - .actual_access:  write_only
        .address_space:  global
        .offset:         40
        .size:           8
        .value_kind:     global_buffer
      - .actual_access:  read_only
        .address_space:  global
        .offset:         48
        .size:           8
        .value_kind:     global_buffer
      - .actual_access:  read_only
        .address_space:  global
        .offset:         56
        .size:           8
        .value_kind:     global_buffer
      - .actual_access:  read_only
        .address_space:  global
        .offset:         64
        .size:           8
        .value_kind:     global_buffer
      - .address_space:  global
        .offset:         72
        .size:           8
        .value_kind:     global_buffer
    .group_segment_fixed_size: 0
    .kernarg_segment_align: 8
    .kernarg_segment_size: 80
    .language:       OpenCL C
    .language_version:
      - 2
      - 0
    .max_flat_workgroup_size: 512
    .name:           _Z11mega_kernelPKfPDF16_PKDF16_S3_S1_PfS0_S0_PK15HIP_vector_typeIfLj2EEPS6_
    .private_segment_fixed_size: 0
    .sgpr_count:     108
    .sgpr_spill_count: 15
    .symbol:         _Z11mega_kernelPKfPDF16_PKDF16_S3_S1_PfS0_S0_PK15HIP_vector_typeIfLj2EEPS6_.kd
    .uniform_work_group_size: 1
    .uses_dynamic_stack: false
    .vgpr_count:     256
    .vgpr_spill_count: 0
    .wavefront_size: 64
